# grouped GEMM epilogue tails: the next unit's 8 row-gate loads use one 32-bit offset + SGPR base + immediate offsets instead of eight VALU-built 64-bit addresses (13 VALU fewer per wave and unit)
# speedup vs baseline: 1.0004x; 1.0004x over previous
.LBB0_1546:
	s_mov_b32 s73, 0xc2700000
	v_mov_b32_e32 v184, 0x41898193
	v_lshlrev_b32_e32 v150, 16, v86
	v_and_b32_e32 v151, 0xffff0000, v86
	v_mul_f32_e32 v158, 0x3d800000, v177
	v_pk_fma_f32 v[130:131], v[158:159], v[130:131], v[150:151] op_sel_hi:[0,1,1]
	v_med3_f32 v130, v130, s73, v184
	v_med3_f32 v131, v131, s73, v184
	v_exp_f32_e64 v178, -v130
	v_exp_f32_e64 v179, -v131
	v_lshlrev_b32_e32 v156, 16, v87
	v_and_b32_e32 v157, 0xffff0000, v87
	v_lshlrev_b32_e32 v152, 16, v82
	v_pk_add_f32 v[178:179], v[178:179], 1.0 op_sel_hi:[1,0]
	v_and_b32_e32 v153, 0xffff0000, v82
	v_lshlrev_b32_e32 v154, 16, v83
	v_and_b32_e32 v155, 0xffff0000, v83
	v_pk_fma_f32 v[132:133], v[158:159], v[132:133], v[156:157] op_sel_hi:[0,1,1]
	v_pk_fma_f32 v[134:135], v[158:159], v[134:135], v[152:153] op_sel_hi:[0,1,1]
	v_pk_fma_f32 v[136:137], v[158:159], v[136:137], v[154:155] op_sel_hi:[0,1,1]
	v_med3_f32 v134, v134, s70, v167
	v_med3_f32 v135, v135, s70, v167
	v_med3_f32 v132, v132, s73, v184
	v_med3_f32 v133, v133, s73, v184
	v_pk_mul_f32 v[130:131], v[130:131], v[134:135]
	v_med3_f32 v134, v136, s70, v167
	v_med3_f32 v135, v137, s70, v167
	v_exp_f32_e64 v136, -v132
	v_exp_f32_e64 v137, -v133
	v_lshlrev_b32_e32 v86, 16, v88
	v_and_b32_e32 v87, 0xffff0000, v88
	v_pk_fma_f32 v[122:123], v[158:159], v[122:123], v[86:87] op_sel_hi:[0,1,1]
	v_pk_add_f32 v[136:137], v[136:137], 1.0 op_sel_hi:[1,0]
	v_med3_f32 v122, v122, s73, v184
	v_pk_mul_f32 v[180:181], v[178:179], v[136:137]
	v_rcp_f32_e32 v180, v180
	v_rcp_f32_e32 v181, v181
	s_nop 0
	v_pk_mul_f32 v[182:183], v[180:181], v[136:137]
	v_pk_mul_f32 v[136:137], v[180:181], v[178:179]
	v_pk_mul_f32 v[130:131], v[130:131], v[182:183]
	v_med3_f32 v123, v123, s73, v184
	v_lshlrev_b32_e32 v88, 16, v89
	v_and_b32_e32 v89, 0xffff0000, v89
	v_pk_mul_f32 v[132:133], v[132:133], v[136:137]
	v_lshlrev_b32_e32 v82, 16, v84
	v_pk_mul_f32 v[132:133], v[132:133], v[134:135]
	v_exp_f32_e64 v134, -v122
	v_exp_f32_e64 v135, -v123
	v_and_b32_e32 v83, 0xffff0000, v84
	v_lshlrev_b32_e32 v84, 16, v85
	v_and_b32_e32 v85, 0xffff0000, v85
	v_pk_add_f32 v[134:135], v[134:135], 1.0 op_sel_hi:[1,0]
	v_pk_fma_f32 v[124:125], v[158:159], v[124:125], v[88:89] op_sel_hi:[0,1,1]
	v_pk_fma_f32 v[126:127], v[158:159], v[126:127], v[82:83] op_sel_hi:[0,1,1]
	v_pk_fma_f32 v[128:129], v[158:159], v[128:129], v[84:85] op_sel_hi:[0,1,1]
	v_med3_f32 v126, v126, s70, v167
	v_med3_f32 v127, v127, s70, v167
	v_med3_f32 v124, v124, s73, v184
	v_med3_f32 v125, v125, s73, v184
	v_pk_mul_f32 v[122:123], v[122:123], v[126:127]
	v_med3_f32 v126, v128, s70, v167
	v_med3_f32 v127, v129, s70, v167
	v_exp_f32_e64 v128, -v124
	v_exp_f32_e64 v129, -v125
	v_mov_b32_e32 v142, v0
	s_and_b64 vcc, exec, s[6:7]
	v_pk_add_f32 v[128:129], v[128:129], 1.0 op_sel_hi:[1,0]
	v_readfirstlane_b32 s69, v142
	v_pk_mul_f32 v[180:181], v[134:135], v[128:129]
	v_rcp_f32_e32 v180, v180
	v_rcp_f32_e32 v181, v181
	s_nop 0
	v_pk_mul_f32 v[182:183], v[180:181], v[128:129]
	v_pk_mul_f32 v[128:129], v[180:181], v[134:135]
	v_pk_mul_f32 v[122:123], v[122:123], v[182:183]
	s_ashr_i32 s8, s69, 6
	s_mul_i32 s9, s8, 0xb00
	s_add_i32 s71, s9, 0
	v_pk_mul_f32 v[124:125], v[124:125], v[128:129]
	v_and_b32_e32 v147, 15, v142
	v_pk_mul_f32 v[124:125], v[124:125], v[126:127]
	v_mov_b32_e32 v126, 0
	v_mov_b32_e32 v127, 0
	v_cvt_pk_fp8_f32 v126, v130, v131
	v_cvt_pk_fp8_f32 v127, v122, v123
	v_lshrrev_b32_e32 v123, 1, v142
	s_add_i32 s71, s71, 0x20000
	v_cvt_pk_fp8_f32 v126, v132, v133 op_sel:[0,0,1]
	v_cvt_pk_fp8_f32 v127, v124, v125 op_sel:[0,0,1]
	v_mul_f32_e32 v124, 0x3d800000, v176
	v_mul_u32_u24_e32 v122, 48, v147
	v_and_b32_e32 v123, 24, v123
	v_pk_fma_f32 v[114:115], v[124:125], v[114:115], v[150:151] op_sel_hi:[0,1,1]
	v_add3_u32 v122, s71, v122, v123
	v_med3_f32 v114, v114, s73, v184
	v_med3_f32 v115, v115, s73, v184
	ds_write_b64 v122, v[126:127]
	v_exp_f32_e64 v126, -v114
	v_exp_f32_e64 v127, -v115
	v_pk_fma_f32 v[116:117], v[124:125], v[116:117], v[156:157] op_sel_hi:[0,1,1]
	v_pk_fma_f32 v[118:119], v[124:125], v[118:119], v[152:153] op_sel_hi:[0,1,1]
	v_pk_fma_f32 v[120:121], v[124:125], v[120:121], v[154:155] op_sel_hi:[0,1,1]
	v_pk_add_f32 v[126:127], v[126:127], 1.0 op_sel_hi:[1,0]
	v_med3_f32 v118, v118, s70, v167
	v_med3_f32 v119, v119, s70, v167
	v_med3_f32 v116, v116, s73, v184
	v_med3_f32 v117, v117, s73, v184
	v_pk_fma_f32 v[106:107], v[124:125], v[106:107], v[86:87] op_sel_hi:[0,1,1]
	v_pk_mul_f32 v[114:115], v[114:115], v[118:119]
	v_med3_f32 v118, v120, s70, v167
	v_med3_f32 v119, v121, s70, v167
	v_exp_f32_e64 v120, -v116
	v_exp_f32_e64 v121, -v117
	v_med3_f32 v106, v106, s73, v184
	v_med3_f32 v107, v107, s73, v184
	v_pk_fma_f32 v[108:109], v[124:125], v[108:109], v[88:89] op_sel_hi:[0,1,1]
	v_pk_add_f32 v[120:121], v[120:121], 1.0 op_sel_hi:[1,0]
	v_pk_fma_f32 v[110:111], v[124:125], v[110:111], v[82:83] op_sel_hi:[0,1,1]
	v_pk_mul_f32 v[180:181], v[126:127], v[120:121]
	v_rcp_f32_e32 v180, v180
	v_rcp_f32_e32 v181, v181
	s_nop 0
	v_pk_mul_f32 v[182:183], v[180:181], v[120:121]
	v_pk_mul_f32 v[120:121], v[180:181], v[126:127]
	v_pk_mul_f32 v[114:115], v[114:115], v[182:183]
	v_pk_fma_f32 v[112:113], v[124:125], v[112:113], v[84:85] op_sel_hi:[0,1,1]
	v_med3_f32 v110, v110, s70, v167
	v_med3_f32 v111, v111, s70, v167
	v_pk_mul_f32 v[116:117], v[116:117], v[120:121]
	v_med3_f32 v108, v108, s73, v184
	v_pk_mul_f32 v[116:117], v[116:117], v[118:119]
	v_exp_f32_e64 v118, -v106
	v_exp_f32_e64 v119, -v107
	v_med3_f32 v109, v109, s73, v184
	s_ashr_i32 s69, s69, 2
	s_andn2_b32 s69, s69, 63
	v_pk_add_f32 v[118:119], v[118:119], 1.0 op_sel_hi:[1,0]
	s_lshl_b32 s8, s8, 5
	s_lshl_b32 s9, s80, 7
	s_and_b32 s8, s8, 0x60
	s_or_b32 s8, s8, s9
	s_ashr_i32 s9, s8, 31
	v_pk_mul_f32 v[106:107], v[106:107], v[110:111]
	v_med3_f32 v110, v112, s70, v167
	v_med3_f32 v111, v113, s70, v167
	v_exp_f32_e64 v112, -v108
	v_exp_f32_e64 v113, -v109
	s_nop 0
	v_pk_add_f32 v[112:113], v[112:113], 1.0 op_sel_hi:[1,0]
	s_nop 0
	v_pk_mul_f32 v[180:181], v[118:119], v[112:113]
	v_rcp_f32_e32 v180, v180
	v_rcp_f32_e32 v181, v181
	s_nop 0
	v_pk_mul_f32 v[182:183], v[180:181], v[112:113]
	v_pk_mul_f32 v[112:113], v[180:181], v[118:119]
	v_pk_mul_f32 v[106:107], v[106:107], v[182:183]
	s_nop 0
	v_pk_mul_f32 v[108:109], v[108:109], v[112:113]
	s_nop 0
	v_pk_mul_f32 v[108:109], v[108:109], v[110:111]
	v_mov_b32_e32 v110, 0
	v_mov_b32_e32 v111, 0
	v_cvt_pk_fp8_f32 v110, v114, v115
	v_cvt_pk_fp8_f32 v111, v106, v107
	v_bfe_u32 v106, v142, 1, 5
	v_mul_u32_u24_e32 v107, 48, v106
	v_cvt_pk_fp8_f32 v110, v116, v117 op_sel:[0,0,1]
	v_cvt_pk_fp8_f32 v111, v108, v109 op_sel:[0,0,1]
	v_lshlrev_b32_e32 v108, 4, v142
	v_and_b32_e32 v142, 16, v108
	v_lshl_or_b32 v106, s78, 8, v106
	ds_write_b64 v122, v[110:111] offset:768
	v_add3_u32 v108, s71, v107, v142
	v_add_u32_e32 v106, s69, v106
	ds_read_b128 v[110:113], v108
	v_ashrrev_i32_e32 v107, 31, v106
	v_lshlrev_b64 v[114:115], 10, v[106:107]
	v_lshl_add_u64 v[114:115], s[16:17], 0, v[114:115]
	v_lshl_add_u64 v[114:115], v[114:115], 0, s[8:9]
	v_lshl_add_u64 v[114:115], v[114:115], 0, v[142:143]
	s_waitcnt lgkmcnt(0)
	global_store_dwordx4 v[114:115], v[110:113], off
	s_nop 1
	v_mul_f32_e32 v110, 0x3d800000, v175
	v_pk_fma_f32 v[98:99], v[110:111], v[98:99], v[150:151] op_sel_hi:[0,1,1]
	v_med3_f32 v98, v98, s73, v184
	v_med3_f32 v99, v99, s73, v184
	v_exp_f32_e64 v112, -v98
	v_exp_f32_e64 v113, -v99
	v_pk_fma_f32 v[100:101], v[110:111], v[100:101], v[156:157] op_sel_hi:[0,1,1]
	v_pk_fma_f32 v[102:103], v[110:111], v[102:103], v[152:153] op_sel_hi:[0,1,1]
	v_pk_fma_f32 v[104:105], v[110:111], v[104:105], v[154:155] op_sel_hi:[0,1,1]
	v_pk_add_f32 v[112:113], v[112:113], 1.0 op_sel_hi:[1,0]
	v_med3_f32 v102, v102, s70, v167
	v_med3_f32 v103, v103, s70, v167
	v_med3_f32 v100, v100, s73, v184
	v_med3_f32 v101, v101, s73, v184
	v_pk_fma_f32 v[90:91], v[110:111], v[90:91], v[86:87] op_sel_hi:[0,1,1]
	v_pk_mul_f32 v[98:99], v[98:99], v[102:103]
	v_med3_f32 v102, v104, s70, v167
	v_med3_f32 v103, v105, s70, v167
	v_exp_f32_e64 v104, -v100
	v_exp_f32_e64 v105, -v101
	v_med3_f32 v90, v90, s73, v184
	v_med3_f32 v91, v91, s73, v184
	v_pk_fma_f32 v[92:93], v[110:111], v[92:93], v[88:89] op_sel_hi:[0,1,1]
	v_pk_add_f32 v[104:105], v[104:105], 1.0 op_sel_hi:[1,0]
	v_pk_fma_f32 v[94:95], v[110:111], v[94:95], v[82:83] op_sel_hi:[0,1,1]
	v_pk_mul_f32 v[180:181], v[112:113], v[104:105]
	v_rcp_f32_e32 v180, v180
	v_rcp_f32_e32 v181, v181
	s_nop 0
	v_pk_mul_f32 v[182:183], v[180:181], v[104:105]
	v_pk_mul_f32 v[104:105], v[180:181], v[112:113]
	v_pk_mul_f32 v[98:99], v[98:99], v[182:183]
	v_pk_fma_f32 v[96:97], v[110:111], v[96:97], v[84:85] op_sel_hi:[0,1,1]
	v_med3_f32 v94, v94, s70, v167
	v_med3_f32 v95, v95, s70, v167
	v_pk_mul_f32 v[100:101], v[100:101], v[104:105]
	v_med3_f32 v92, v92, s73, v184
	v_pk_mul_f32 v[100:101], v[100:101], v[102:103]
	v_exp_f32_e64 v102, -v90
	v_exp_f32_e64 v103, -v91
	v_med3_f32 v93, v93, s73, v184
	v_pk_add_f32 v[102:103], v[102:103], 1.0 op_sel_hi:[1,0]
	s_nop 0
	s_nop 0
	s_nop 0
	v_pk_mul_f32 v[90:91], v[90:91], v[94:95]
	v_med3_f32 v94, v96, s70, v167
	v_med3_f32 v95, v97, s70, v167
	v_exp_f32_e64 v96, -v92
	v_exp_f32_e64 v97, -v93
	s_nop 0
	v_pk_add_f32 v[96:97], v[96:97], 1.0 op_sel_hi:[1,0]
	s_nop 0
	v_pk_mul_f32 v[180:181], v[102:103], v[96:97]
	v_rcp_f32_e32 v180, v180
	v_rcp_f32_e32 v181, v181
	s_nop 0
	v_pk_mul_f32 v[182:183], v[180:181], v[96:97]
	v_pk_mul_f32 v[96:97], v[180:181], v[102:103]
	v_pk_mul_f32 v[90:91], v[90:91], v[182:183]
	s_nop 0
	v_pk_mul_f32 v[92:93], v[92:93], v[96:97]
	s_nop 0
	v_pk_mul_f32 v[92:93], v[92:93], v[94:95]
	v_mov_b32_e32 v95, v143
	v_cvt_pk_fp8_f32 v95, v90, v91
	v_mul_f32_e32 v90, 0x3d800000, v174
	v_pk_fma_f32 v[74:75], v[90:91], v[74:75], v[150:151] op_sel_hi:[0,1,1]
	v_med3_f32 v74, v74, s73, v184
	v_med3_f32 v75, v75, s73, v184
	v_cvt_pk_fp8_f32 v95, v92, v93 op_sel:[0,0,1]
	v_exp_f32_e64 v92, -v74
	v_exp_f32_e64 v93, -v75
	v_pk_fma_f32 v[76:77], v[90:91], v[76:77], v[156:157] op_sel_hi:[0,1,1]
	v_pk_fma_f32 v[78:79], v[90:91], v[78:79], v[152:153] op_sel_hi:[0,1,1]
	v_pk_fma_f32 v[80:81], v[90:91], v[80:81], v[154:155] op_sel_hi:[0,1,1]
	v_pk_add_f32 v[92:93], v[92:93], 1.0 op_sel_hi:[1,0]
	v_med3_f32 v78, v78, s70, v167
	v_med3_f32 v79, v79, s70, v167
	v_med3_f32 v76, v76, s73, v184
	v_med3_f32 v77, v77, s73, v184
	v_pk_fma_f32 v[66:67], v[90:91], v[66:67], v[86:87] op_sel_hi:[0,1,1]
	v_pk_mul_f32 v[74:75], v[74:75], v[78:79]
	v_med3_f32 v78, v80, s70, v167
	v_med3_f32 v79, v81, s70, v167
	v_exp_f32_e64 v80, -v76
	v_exp_f32_e64 v81, -v77
	v_med3_f32 v66, v66, s73, v184
	v_med3_f32 v67, v67, s73, v184
	v_pk_fma_f32 v[68:69], v[90:91], v[68:69], v[88:89] op_sel_hi:[0,1,1]
	v_pk_add_f32 v[80:81], v[80:81], 1.0 op_sel_hi:[1,0]
	v_pk_fma_f32 v[70:71], v[90:91], v[70:71], v[82:83] op_sel_hi:[0,1,1]
	v_pk_mul_f32 v[180:181], v[92:93], v[80:81]
	v_rcp_f32_e32 v180, v180
	v_rcp_f32_e32 v181, v181
	s_nop 0
	v_pk_mul_f32 v[182:183], v[180:181], v[80:81]
	v_pk_mul_f32 v[80:81], v[180:181], v[92:93]
	v_pk_mul_f32 v[74:75], v[74:75], v[182:183]
	v_pk_fma_f32 v[72:73], v[90:91], v[72:73], v[84:85] op_sel_hi:[0,1,1]
	v_med3_f32 v70, v70, s70, v167
	v_med3_f32 v71, v71, s70, v167
	v_pk_mul_f32 v[76:77], v[76:77], v[80:81]
	v_med3_f32 v68, v68, s73, v184
	v_pk_mul_f32 v[76:77], v[76:77], v[78:79]
	v_exp_f32_e64 v78, -v66
	v_exp_f32_e64 v79, -v67
	v_med3_f32 v69, v69, s73, v184
	v_mov_b32_e32 v94, v143
	v_cvt_pk_fp8_f32 v94, v98, v99
	v_pk_add_f32 v[78:79], v[78:79], 1.0 op_sel_hi:[1,0]
	v_cvt_pk_fp8_f32 v94, v100, v101 op_sel:[0,0,1]
	ds_write_b64 v122, v[94:95]
	s_nop 0
	v_pk_mul_f32 v[66:67], v[66:67], v[70:71]
	v_med3_f32 v70, v72, s70, v167
	v_med3_f32 v71, v73, s70, v167
	v_exp_f32_e64 v72, -v68
	v_exp_f32_e64 v73, -v69
	s_nop 0
	v_pk_add_f32 v[72:73], v[72:73], 1.0 op_sel_hi:[1,0]
	s_nop 0
	v_pk_mul_f32 v[180:181], v[78:79], v[72:73]
	v_rcp_f32_e32 v180, v180
	v_rcp_f32_e32 v181, v181
	s_nop 0
	v_pk_mul_f32 v[182:183], v[180:181], v[72:73]
	v_pk_mul_f32 v[72:73], v[180:181], v[78:79]
	v_pk_mul_f32 v[66:67], v[66:67], v[182:183]
	s_nop 0
	v_pk_mul_f32 v[68:69], v[68:69], v[72:73]
	s_nop 0
	v_pk_mul_f32 v[68:69], v[68:69], v[70:71]
	v_mov_b32_e32 v70, v143
	v_mov_b32_e32 v71, v143
	v_cvt_pk_fp8_f32 v70, v74, v75
	v_cvt_pk_fp8_f32 v71, v66, v67
	v_cvt_pk_fp8_f32 v70, v76, v77 op_sel:[0,0,1]
	v_cvt_pk_fp8_f32 v71, v68, v69 op_sel:[0,0,1]
	ds_write_b64 v122, v[70:71] offset:768
	v_or_b32_e32 v70, 32, v106
	ds_read_b128 v[66:69], v108
	v_ashrrev_i32_e32 v71, 31, v70
	v_lshlrev_b64 v[70:71], 10, v[70:71]
	v_lshl_add_u64 v[70:71], s[16:17], 0, v[70:71]
	v_lshl_add_u64 v[70:71], v[70:71], 0, s[8:9]
	v_lshl_add_u64 v[70:71], v[70:71], 0, v[142:143]
	s_waitcnt lgkmcnt(0)
	global_store_dwordx4 v[70:71], v[66:69], off
	s_nop 1
	v_mul_f32_e32 v66, 0x3d800000, v173
	v_pk_fma_f32 v[58:59], v[66:67], v[58:59], v[150:151] op_sel_hi:[0,1,1]
	v_med3_f32 v58, v58, s73, v184
	v_med3_f32 v59, v59, s73, v184
	v_exp_f32_e64 v68, -v58
	v_exp_f32_e64 v69, -v59
	v_pk_fma_f32 v[60:61], v[66:67], v[60:61], v[156:157] op_sel_hi:[0,1,1]
	v_pk_fma_f32 v[62:63], v[66:67], v[62:63], v[152:153] op_sel_hi:[0,1,1]
	v_pk_fma_f32 v[64:65], v[66:67], v[64:65], v[154:155] op_sel_hi:[0,1,1]
	v_pk_add_f32 v[68:69], v[68:69], 1.0 op_sel_hi:[1,0]
	v_med3_f32 v62, v62, s70, v167
	v_med3_f32 v63, v63, s70, v167
	v_med3_f32 v60, v60, s73, v184
	v_med3_f32 v61, v61, s73, v184
	v_pk_fma_f32 v[50:51], v[66:67], v[50:51], v[86:87] op_sel_hi:[0,1,1]
	v_pk_mul_f32 v[58:59], v[58:59], v[62:63]
	v_med3_f32 v62, v64, s70, v167
	v_med3_f32 v63, v65, s70, v167
	v_exp_f32_e64 v64, -v60
	v_exp_f32_e64 v65, -v61
	v_med3_f32 v50, v50, s73, v184
	v_med3_f32 v51, v51, s73, v184
	v_pk_fma_f32 v[52:53], v[66:67], v[52:53], v[88:89] op_sel_hi:[0,1,1]
	v_pk_add_f32 v[64:65], v[64:65], 1.0 op_sel_hi:[1,0]
	v_pk_fma_f32 v[54:55], v[66:67], v[54:55], v[82:83] op_sel_hi:[0,1,1]
	v_pk_mul_f32 v[180:181], v[68:69], v[64:65]
	v_rcp_f32_e32 v180, v180
	v_rcp_f32_e32 v181, v181
	s_nop 0
	v_pk_mul_f32 v[182:183], v[180:181], v[64:65]
	v_pk_mul_f32 v[64:65], v[180:181], v[68:69]
	v_pk_mul_f32 v[58:59], v[58:59], v[182:183]
	v_pk_fma_f32 v[56:57], v[66:67], v[56:57], v[84:85] op_sel_hi:[0,1,1]
	v_med3_f32 v54, v54, s70, v167
	v_med3_f32 v55, v55, s70, v167
	v_pk_mul_f32 v[60:61], v[60:61], v[64:65]
	v_med3_f32 v52, v52, s73, v184
	v_pk_mul_f32 v[60:61], v[60:61], v[62:63]
	v_exp_f32_e64 v62, -v50
	v_exp_f32_e64 v63, -v51
	v_med3_f32 v53, v53, s73, v184
	v_pk_add_f32 v[62:63], v[62:63], 1.0 op_sel_hi:[1,0]
	s_nop 0
	s_nop 0
	s_nop 0
	v_pk_mul_f32 v[50:51], v[50:51], v[54:55]
	v_med3_f32 v54, v56, s70, v167
	v_med3_f32 v55, v57, s70, v167
	v_exp_f32_e64 v56, -v52
	v_exp_f32_e64 v57, -v53
	s_nop 0
	v_pk_add_f32 v[56:57], v[56:57], 1.0 op_sel_hi:[1,0]
	s_nop 0
	v_pk_mul_f32 v[180:181], v[62:63], v[56:57]
	v_rcp_f32_e32 v180, v180
	v_rcp_f32_e32 v181, v181
	s_nop 0
	v_pk_mul_f32 v[182:183], v[180:181], v[56:57]
	v_pk_mul_f32 v[56:57], v[180:181], v[62:63]
	v_pk_mul_f32 v[50:51], v[50:51], v[182:183]
	s_nop 0
	v_pk_mul_f32 v[52:53], v[52:53], v[56:57]
	s_nop 0
	v_pk_mul_f32 v[52:53], v[52:53], v[54:55]
	v_mov_b32_e32 v55, v143
	v_cvt_pk_fp8_f32 v55, v50, v51
	v_mul_f32_e32 v50, 0x3d800000, v172
	v_pk_fma_f32 v[42:43], v[50:51], v[42:43], v[150:151] op_sel_hi:[0,1,1]
	v_med3_f32 v42, v42, s73, v184
	v_med3_f32 v43, v43, s73, v184
	v_cvt_pk_fp8_f32 v55, v52, v53 op_sel:[0,0,1]
	v_exp_f32_e64 v52, -v42
	v_exp_f32_e64 v53, -v43
	v_pk_fma_f32 v[44:45], v[50:51], v[44:45], v[156:157] op_sel_hi:[0,1,1]
	v_pk_fma_f32 v[46:47], v[50:51], v[46:47], v[152:153] op_sel_hi:[0,1,1]
	v_pk_fma_f32 v[48:49], v[50:51], v[48:49], v[154:155] op_sel_hi:[0,1,1]
	v_pk_add_f32 v[52:53], v[52:53], 1.0 op_sel_hi:[1,0]
	v_med3_f32 v46, v46, s70, v167
	v_med3_f32 v47, v47, s70, v167
	v_med3_f32 v44, v44, s73, v184
	v_med3_f32 v45, v45, s73, v184
	v_pk_fma_f32 v[34:35], v[50:51], v[34:35], v[86:87] op_sel_hi:[0,1,1]
	v_pk_mul_f32 v[42:43], v[42:43], v[46:47]
	v_med3_f32 v46, v48, s70, v167
	v_med3_f32 v47, v49, s70, v167
	v_exp_f32_e64 v48, -v44
	v_exp_f32_e64 v49, -v45
	v_med3_f32 v34, v34, s73, v184
	v_med3_f32 v35, v35, s73, v184
	v_pk_fma_f32 v[36:37], v[50:51], v[36:37], v[88:89] op_sel_hi:[0,1,1]
	v_pk_add_f32 v[48:49], v[48:49], 1.0 op_sel_hi:[1,0]
	v_pk_fma_f32 v[38:39], v[50:51], v[38:39], v[82:83] op_sel_hi:[0,1,1]
	v_pk_mul_f32 v[180:181], v[52:53], v[48:49]
	v_rcp_f32_e32 v180, v180
	v_rcp_f32_e32 v181, v181
	s_nop 0
	v_pk_mul_f32 v[182:183], v[180:181], v[48:49]
	v_pk_mul_f32 v[48:49], v[180:181], v[52:53]
	v_pk_mul_f32 v[42:43], v[42:43], v[182:183]
	v_pk_fma_f32 v[40:41], v[50:51], v[40:41], v[84:85] op_sel_hi:[0,1,1]
	v_med3_f32 v38, v38, s70, v167
	v_med3_f32 v39, v39, s70, v167
	v_pk_mul_f32 v[44:45], v[44:45], v[48:49]
	v_med3_f32 v36, v36, s73, v184
	v_pk_mul_f32 v[44:45], v[44:45], v[46:47]
	v_exp_f32_e64 v46, -v34
	v_exp_f32_e64 v47, -v35
	v_med3_f32 v37, v37, s73, v184
	v_mov_b32_e32 v54, v143
	v_cvt_pk_fp8_f32 v54, v58, v59
	v_pk_add_f32 v[46:47], v[46:47], 1.0 op_sel_hi:[1,0]
	v_cvt_pk_fp8_f32 v54, v60, v61 op_sel:[0,0,1]
	ds_write_b64 v122, v[54:55]
	s_nop 0
	v_pk_mul_f32 v[34:35], v[34:35], v[38:39]
	v_med3_f32 v38, v40, s70, v167
	v_med3_f32 v39, v41, s70, v167
	v_exp_f32_e64 v40, -v36
	v_exp_f32_e64 v41, -v37
	s_nop 0
	v_pk_add_f32 v[40:41], v[40:41], 1.0 op_sel_hi:[1,0]
	s_nop 0
	v_pk_mul_f32 v[180:181], v[46:47], v[40:41]
	v_rcp_f32_e32 v180, v180
	v_rcp_f32_e32 v181, v181
	s_nop 0
	v_pk_mul_f32 v[182:183], v[180:181], v[40:41]
	v_pk_mul_f32 v[40:41], v[180:181], v[46:47]
	v_pk_mul_f32 v[34:35], v[34:35], v[182:183]
	s_nop 0
	v_pk_mul_f32 v[36:37], v[36:37], v[40:41]
	s_nop 0
	v_pk_mul_f32 v[36:37], v[36:37], v[38:39]
	v_mov_b32_e32 v38, v143
	v_mov_b32_e32 v39, v143
	v_cvt_pk_fp8_f32 v38, v42, v43
	v_cvt_pk_fp8_f32 v39, v34, v35
	v_cvt_pk_fp8_f32 v38, v44, v45 op_sel:[0,0,1]
	v_cvt_pk_fp8_f32 v39, v36, v37 op_sel:[0,0,1]
	ds_write_b64 v122, v[38:39] offset:768
	v_add_u32_e32 v38, 0x80, v106
	ds_read_b128 v[34:37], v108
	v_ashrrev_i32_e32 v39, 31, v38
	v_lshlrev_b64 v[38:39], 10, v[38:39]
	v_lshl_add_u64 v[38:39], s[16:17], 0, v[38:39]
	v_lshl_add_u64 v[38:39], v[38:39], 0, s[8:9]
	v_lshl_add_u64 v[38:39], v[38:39], 0, v[142:143]
	s_waitcnt lgkmcnt(0)
	global_store_dwordx4 v[38:39], v[34:37], off
	s_nop 1
	v_mul_f32_e32 v34, 0x3d800000, v171
	v_pk_fma_f32 v[26:27], v[34:35], v[26:27], v[150:151] op_sel_hi:[0,1,1]
	v_med3_f32 v26, v26, s73, v184
	v_med3_f32 v27, v27, s73, v184
	v_exp_f32_e64 v36, -v26
	v_exp_f32_e64 v37, -v27
	v_pk_fma_f32 v[28:29], v[34:35], v[28:29], v[156:157] op_sel_hi:[0,1,1]
	v_pk_fma_f32 v[30:31], v[34:35], v[30:31], v[152:153] op_sel_hi:[0,1,1]
	v_pk_fma_f32 v[32:33], v[34:35], v[32:33], v[154:155] op_sel_hi:[0,1,1]
	v_pk_add_f32 v[36:37], v[36:37], 1.0 op_sel_hi:[1,0]
	v_med3_f32 v30, v30, s70, v167
	v_med3_f32 v31, v31, s70, v167
	v_med3_f32 v28, v28, s73, v184
	v_med3_f32 v29, v29, s73, v184
	v_pk_fma_f32 v[18:19], v[34:35], v[18:19], v[86:87] op_sel_hi:[0,1,1]
	v_pk_mul_f32 v[26:27], v[26:27], v[30:31]
	v_med3_f32 v30, v32, s70, v167
	v_med3_f32 v31, v33, s70, v167
	v_exp_f32_e64 v32, -v28
	v_exp_f32_e64 v33, -v29
	v_med3_f32 v18, v18, s73, v184
	v_med3_f32 v19, v19, s73, v184
	v_pk_fma_f32 v[20:21], v[34:35], v[20:21], v[88:89] op_sel_hi:[0,1,1]
	v_pk_add_f32 v[32:33], v[32:33], 1.0 op_sel_hi:[1,0]
	v_pk_fma_f32 v[22:23], v[34:35], v[22:23], v[82:83] op_sel_hi:[0,1,1]
	v_pk_mul_f32 v[180:181], v[36:37], v[32:33]
	v_rcp_f32_e32 v180, v180
	v_rcp_f32_e32 v181, v181
	s_nop 0
	v_pk_mul_f32 v[182:183], v[180:181], v[32:33]
	v_pk_mul_f32 v[32:33], v[180:181], v[36:37]
	v_pk_mul_f32 v[26:27], v[26:27], v[182:183]
	v_pk_fma_f32 v[24:25], v[34:35], v[24:25], v[84:85] op_sel_hi:[0,1,1]
	v_med3_f32 v22, v22, s70, v167
	v_med3_f32 v23, v23, s70, v167
	v_pk_mul_f32 v[28:29], v[28:29], v[32:33]
	v_med3_f32 v20, v20, s73, v184
	v_pk_mul_f32 v[28:29], v[28:29], v[30:31]
	v_exp_f32_e64 v30, -v18
	v_exp_f32_e64 v31, -v19
	v_med3_f32 v21, v21, s73, v184
	v_pk_add_f32 v[30:31], v[30:31], 1.0 op_sel_hi:[1,0]
	s_nop 0
	s_nop 0
	s_nop 0
	v_pk_mul_f32 v[18:19], v[18:19], v[22:23]
	v_med3_f32 v22, v24, s70, v167
	v_med3_f32 v23, v25, s70, v167
	v_exp_f32_e64 v24, -v20
	v_exp_f32_e64 v25, -v21
	s_nop 0
	v_pk_add_f32 v[24:25], v[24:25], 1.0 op_sel_hi:[1,0]
	s_nop 0
	v_pk_mul_f32 v[180:181], v[30:31], v[24:25]
	v_rcp_f32_e32 v180, v180
	v_rcp_f32_e32 v181, v181
	s_nop 0
	v_pk_mul_f32 v[182:183], v[180:181], v[24:25]
	v_pk_mul_f32 v[24:25], v[180:181], v[30:31]
	v_pk_mul_f32 v[18:19], v[18:19], v[182:183]
	s_nop 0
	v_pk_mul_f32 v[20:21], v[20:21], v[24:25]
	s_nop 0
	v_pk_mul_f32 v[20:21], v[20:21], v[22:23]
	v_mov_b32_e32 v23, v143
	v_cvt_pk_fp8_f32 v23, v18, v19
	v_mul_f32_e32 v18, 0x3d800000, v168
	v_pk_fma_f32 v[10:11], v[18:19], v[10:11], v[150:151] op_sel_hi:[0,1,1]
	v_med3_f32 v10, v10, s73, v184
	v_med3_f32 v11, v11, s73, v184
	v_cvt_pk_fp8_f32 v23, v20, v21 op_sel:[0,0,1]
	v_exp_f32_e64 v20, -v10
	v_exp_f32_e64 v21, -v11
	v_pk_fma_f32 v[12:13], v[18:19], v[12:13], v[156:157] op_sel_hi:[0,1,1]
	v_pk_fma_f32 v[14:15], v[18:19], v[14:15], v[152:153] op_sel_hi:[0,1,1]
	v_pk_fma_f32 v[16:17], v[18:19], v[16:17], v[154:155] op_sel_hi:[0,1,1]
	v_pk_add_f32 v[20:21], v[20:21], 1.0 op_sel_hi:[1,0]
	v_med3_f32 v14, v14, s70, v167
	v_med3_f32 v15, v15, s70, v167
	v_med3_f32 v12, v12, s73, v184
	v_med3_f32 v13, v13, s73, v184
	v_pk_fma_f32 v[2:3], v[18:19], v[2:3], v[86:87] op_sel_hi:[0,1,1]
	v_pk_mul_f32 v[10:11], v[10:11], v[14:15]
	v_med3_f32 v14, v16, s70, v167
	v_med3_f32 v15, v17, s70, v167
	v_exp_f32_e64 v16, -v12
	v_exp_f32_e64 v17, -v13
	v_med3_f32 v2, v2, s73, v184
	v_med3_f32 v3, v3, s73, v184
	v_pk_fma_f32 v[4:5], v[18:19], v[4:5], v[88:89] op_sel_hi:[0,1,1]
	v_pk_add_f32 v[16:17], v[16:17], 1.0 op_sel_hi:[1,0]
	v_pk_fma_f32 v[6:7], v[18:19], v[6:7], v[82:83] op_sel_hi:[0,1,1]
	v_pk_mul_f32 v[180:181], v[20:21], v[16:17]
	v_rcp_f32_e32 v180, v180
	v_rcp_f32_e32 v181, v181
	s_nop 0
	v_pk_mul_f32 v[182:183], v[180:181], v[16:17]
	v_pk_mul_f32 v[16:17], v[180:181], v[20:21]
	v_pk_mul_f32 v[10:11], v[10:11], v[182:183]
	v_pk_fma_f32 v[8:9], v[18:19], v[8:9], v[84:85] op_sel_hi:[0,1,1]
	v_med3_f32 v6, v6, s70, v167
	v_med3_f32 v7, v7, s70, v167
	v_pk_mul_f32 v[12:13], v[12:13], v[16:17]
	v_med3_f32 v4, v4, s73, v184
	v_pk_mul_f32 v[12:13], v[12:13], v[14:15]
	v_exp_f32_e64 v14, -v2
	v_exp_f32_e64 v15, -v3
	v_med3_f32 v5, v5, s73, v184
	v_mov_b32_e32 v22, v143
	v_cvt_pk_fp8_f32 v22, v26, v27
	v_pk_add_f32 v[14:15], v[14:15], 1.0 op_sel_hi:[1,0]
	v_cvt_pk_fp8_f32 v22, v28, v29 op_sel:[0,0,1]
	ds_write_b64 v122, v[22:23]
	s_nop 0
	v_pk_mul_f32 v[2:3], v[2:3], v[6:7]
	v_med3_f32 v6, v8, s70, v167
	v_med3_f32 v7, v9, s70, v167
	v_exp_f32_e64 v8, -v4
	v_exp_f32_e64 v9, -v5
	s_nop 0
	v_pk_add_f32 v[8:9], v[8:9], 1.0 op_sel_hi:[1,0]
	s_nop 0
	v_pk_mul_f32 v[180:181], v[14:15], v[8:9]
	v_rcp_f32_e32 v180, v180
	v_rcp_f32_e32 v181, v181
	s_nop 0
	v_pk_mul_f32 v[182:183], v[180:181], v[8:9]
	v_pk_mul_f32 v[8:9], v[180:181], v[14:15]
	v_pk_mul_f32 v[2:3], v[2:3], v[182:183]
	s_nop 0
	v_pk_mul_f32 v[4:5], v[4:5], v[8:9]
	s_nop 0
	v_pk_mul_f32 v[4:5], v[4:5], v[6:7]
	v_mov_b32_e32 v6, v143
	v_mov_b32_e32 v7, v143
	v_cvt_pk_fp8_f32 v6, v10, v11
	v_cvt_pk_fp8_f32 v7, v2, v3
	v_cvt_pk_fp8_f32 v6, v12, v13 op_sel:[0,0,1]
	v_cvt_pk_fp8_f32 v7, v4, v5 op_sel:[0,0,1]
	ds_write_b64 v122, v[6:7] offset:768
	v_add_u32_e32 v6, 0xa0, v106
	ds_read_b128 v[2:5], v108
	v_ashrrev_i32_e32 v7, 31, v6
	v_lshlrev_b64 v[6:7], 10, v[6:7]
	v_lshl_add_u64 v[6:7], s[16:17], 0, v[6:7]
	v_lshl_add_u64 v[6:7], v[6:7], 0, s[8:9]
	v_lshl_add_u64 v[6:7], v[6:7], 0, v[142:143]
	s_mov_b64 s[8:9], -1
	s_waitcnt lgkmcnt(0)
	global_store_dwordx4 v[6:7], v[2:5], off
	s_cbranch_vccnz .LBB0_1537
	s_lshl_b64 s[6:7], s[74:75], 12
	s_add_u32 s9, s33, s6
	s_addc_u32 s69, s54, s7
	s_lshl_b32 s6, s68, 7
	s_ashr_i32 s7, s6, 31
	v_mov_b32_e32 v2, v0
	s_lshl_b64 s[6:7], s[6:7], 1
	s_add_u32 s6, s9, s6
	v_readfirstlane_b32 s8, v2
	s_addc_u32 s7, s69, s7
	s_and_b32 s9, s8, 0xc0
	s_add_u32 s6, s6, s9
	s_addc_u32 s7, s7, 0
	v_and_b32_e32 v3, 48, v2
	global_load_dwordx4 v[86:89], v3, s[6:7]
	global_load_dwordx4 v[82:85], v3, s[6:7] offset:2048
	s_ashr_i32 s7, s8, 2
	s_lshl_b32 s6, s72, 8
	s_andn2_b32 s7, s7, 63
	s_add_i32 s7, s7, s6
	v_and_or_b32 v2, v2, 15, s7
	v_lshlrev_b32_e32 v4, 2, v2
	global_load_dword v177, v4, s[12:13] offset:0
	global_load_dword v176, v4, s[12:13] offset:64
	global_load_dword v175, v4, s[12:13] offset:128
	global_load_dword v174, v4, s[12:13] offset:192
	global_load_dword v173, v4, s[12:13] offset:512
	global_load_dword v172, v4, s[12:13] offset:576
	global_load_dword v171, v4, s[12:13] offset:640
	global_load_dword v168, v4, s[12:13] offset:704
	s_andn2_b64 vcc, exec, s[14:15]
	s_cbranch_vccnz .LBB0_1536
	s_barrier
	s_branch .LBB0_1536

.LBB0_1627:
	v_lshlrev_b32_e32 v158, 16, v6
	v_and_b32_e32 v159, 0xffff0000, v6
	v_lshlrev_b32_e32 v154, 16, v8
	v_and_b32_e32 v155, 0xffff0000, v8
	v_lshlrev_b32_e32 v156, 16, v7
	v_and_b32_e32 v157, 0xffff0000, v7
	v_lshlrev_b32_e32 v152, 16, v9
	v_and_b32_e32 v153, 0xffff0000, v9
	s_waitcnt vmcnt(10)
	v_lshlrev_b32_e32 v6, 16, v4
	v_and_b32_e32 v7, 0xffff0000, v4
	v_mul_f32_e32 v4, 0x41000000, v146
	v_pk_fma_f32 v[134:135], v[134:135], s[36:37], v[158:159] op_sel_hi:[1,0,1]
	v_pk_fma_f32 v[130:131], v[130:131], s[36:37], v[154:155] op_sel_hi:[1,0,1]
	v_pk_fma_f32 v[136:137], v[136:137], s[36:37], v[156:157] op_sel_hi:[1,0,1]
	v_pk_mul_f32 v[134:135], v[4:5], v[134:135] op_sel_hi:[0,1]
	v_pk_fma_f32 v[132:133], v[132:133], s[36:37], v[152:153] op_sel_hi:[1,0,1]
	v_pk_mul_f32 v[130:131], v[4:5], v[130:131] op_sel_hi:[0,1]
	v_lshlrev_b32_e32 v150, 16, v2
	v_and_b32_e32 v151, 0xffff0000, v2
	v_lshlrev_b32_e32 v8, 16, v3
	v_and_b32_e32 v9, 0xffff0000, v3
	v_lshlrev_b32_e32 v2, 16, v5
	v_and_b32_e32 v3, 0xffff0000, v5
	v_pk_mul_f32 v[136:137], v[4:5], v[136:137] op_sel_hi:[0,1]
	v_pk_mul_f32 v[132:133], v[4:5], v[132:133] op_sel_hi:[0,1]
	v_med3_f32 v5, v134, s70, v164
	v_med3_f32 v134, v130, s70, v164
	v_med3_f32 v135, v135, s70, v164
	v_mov_b32_e32 v130, 0
	v_cvt_pk_fp8_f32 v130, v5, v135
	v_med3_f32 v136, v136, s70, v164
	v_med3_f32 v5, v137, s70, v164
	v_pk_fma_f32 v[126:127], v[126:127], s[36:37], v[150:151] op_sel_hi:[1,0,1]
	v_pk_fma_f32 v[128:129], v[128:129], s[36:37], v[8:9] op_sel_hi:[1,0,1]
	v_pk_fma_f32 v[122:123], v[122:123], s[36:37], v[6:7] op_sel_hi:[1,0,1]
	v_pk_fma_f32 v[124:125], v[124:125], s[36:37], v[2:3] op_sel_hi:[1,0,1]
	v_cvt_pk_fp8_f32 v130, v136, v5 op_sel:[0,0,1]
	v_pk_mul_f32 v[128:129], v[4:5], v[128:129] op_sel_hi:[0,1]
	v_pk_mul_f32 v[126:127], v[4:5], v[126:127] op_sel_hi:[0,1]
	v_pk_mul_f32 v[124:125], v[4:5], v[124:125] op_sel_hi:[0,1]
	v_pk_mul_f32 v[4:5], v[4:5], v[122:123] op_sel_hi:[0,1]
	v_med3_f32 v146, v131, s70, v164
	v_mov_b32_e32 v131, 0
	v_med3_f32 v122, v126, s70, v164
	v_med3_f32 v123, v4, s70, v164
	v_med3_f32 v126, v127, s70, v164
	v_med3_f32 v127, v5, s70, v164
	v_mov_b32_e32 v4, 0
	v_mov_b32_e32 v5, 0
	v_cvt_pk_fp8_f32 v131, v134, v146
	v_cvt_pk_fp8_f32 v4, v122, v126
	v_cvt_pk_fp8_f32 v5, v123, v127
	v_mov_b32_e32 v171, v0
	v_med3_f32 v132, v132, s70, v164
	v_readfirstlane_b32 s39, v171
	s_lshr_b32 s6, s39, 6
	v_med3_f32 v133, v133, s70, v164
	v_med3_f32 v128, v128, s70, v164
	v_med3_f32 v124, v124, s70, v164
	v_med3_f32 v122, v129, s70, v164
	v_med3_f32 v123, v125, s70, v164
	s_mulk_i32 s6, 0xb00
	v_cvt_pk_fp8_f32 v131, v132, v133 op_sel:[0,0,1]
	v_cvt_pk_fp8_f32 v4, v128, v122 op_sel:[0,0,1]
	v_cvt_pk_fp8_f32 v5, v124, v123 op_sel:[0,0,1]
	s_add_i32 s6, s6, 0
	v_and_b32_e32 v172, 15, v171
	v_lshrrev_b32_e32 v123, 1, v171
	s_add_i32 s41, s6, 0x20000
	v_mul_u32_u24_e32 v122, 0x50, v172
	v_and_b32_e32 v123, 24, v123
	v_add3_u32 v122, s41, v122, v123
	s_and_b32 s7, s39, 0xc0
	ds_write2_b64 v122, v[130:131], v[4:5] offset1:4
	v_bfe_u32 v4, v171, 2, 4
	s_ashr_i32 s39, s39, 2
	v_mul_u32_u24_e32 v5, 0x50, v4
	v_lshlrev_b32_e32 v123, 4, v171
	s_andn2_b32 s39, s39, 63
	v_lshl_or_b32 v4, s48, 8, v4
	v_and_b32_e32 v146, 48, v123
	v_add_u32_e32 v4, s39, v4
	v_mul_f32_e32 v130, 0x41000000, v170
	v_pk_fma_f32 v[118:119], v[118:119], s[36:37], v[158:159] op_sel_hi:[1,0,1]
	v_pk_fma_f32 v[114:115], v[114:115], s[36:37], v[154:155] op_sel_hi:[1,0,1]
	v_add3_u32 v123, s41, v5, v146
	v_ashrrev_i32_e32 v5, 31, v4
	v_pk_mul_f32 v[118:119], v[130:131], v[118:119] op_sel_hi:[0,1]
	v_pk_mul_f32 v[114:115], v[130:131], v[114:115] op_sel_hi:[0,1]
	v_lshlrev_b64 v[128:129], 10, v[4:5]
	v_med3_f32 v5, v118, s70, v164
	v_med3_f32 v118, v114, s70, v164
	v_med3_f32 v119, v119, s70, v164
	v_mov_b32_e32 v114, v147
	v_cvt_pk_fp8_f32 v114, v5, v119
	v_pk_fma_f32 v[120:121], v[120:121], s[36:37], v[156:157] op_sel_hi:[1,0,1]
	v_pk_fma_f32 v[116:117], v[116:117], s[36:37], v[152:153] op_sel_hi:[1,0,1]
	v_pk_mul_f32 v[120:121], v[130:131], v[120:121] op_sel_hi:[0,1]
	v_pk_mul_f32 v[116:117], v[130:131], v[116:117] op_sel_hi:[0,1]
	v_med3_f32 v131, v115, s70, v164
	v_pk_fma_f32 v[110:111], v[110:111], s[36:37], v[150:151] op_sel_hi:[1,0,1]
	v_pk_fma_f32 v[106:107], v[106:107], s[36:37], v[6:7] op_sel_hi:[1,0,1]
	v_med3_f32 v120, v120, s70, v164
	v_med3_f32 v5, v121, s70, v164
	v_pk_mul_f32 v[110:111], v[130:131], v[110:111] op_sel_hi:[0,1]
	v_pk_mul_f32 v[106:107], v[130:131], v[106:107] op_sel_hi:[0,1]
	v_cvt_pk_fp8_f32 v114, v120, v5 op_sel:[0,0,1]
	v_med3_f32 v5, v110, s70, v164
	v_med3_f32 v110, v106, s70, v164
	v_med3_f32 v111, v111, s70, v164
	v_mov_b32_e32 v106, v147
	v_cvt_pk_fp8_f32 v106, v5, v111
	v_pk_fma_f32 v[112:113], v[112:113], s[36:37], v[8:9] op_sel_hi:[1,0,1]
	v_mov_b32_e32 v115, v147
	v_pk_mul_f32 v[112:113], v[130:131], v[112:113] op_sel_hi:[0,1]
	v_med3_f32 v112, v112, s70, v164
	v_med3_f32 v5, v113, s70, v164
	v_cvt_pk_fp8_f32 v106, v112, v5 op_sel:[0,0,1]
	v_mul_f32_e32 v112, 0x41000000, v169
	v_pk_fma_f32 v[102:103], v[102:103], s[36:37], v[158:159] op_sel_hi:[1,0,1]
	v_pk_fma_f32 v[98:99], v[98:99], s[36:37], v[154:155] op_sel_hi:[1,0,1]
	v_cvt_pk_fp8_f32 v115, v118, v131
	v_pk_mul_f32 v[102:103], v[112:113], v[102:103] op_sel_hi:[0,1]
	v_pk_mul_f32 v[98:99], v[112:113], v[98:99] op_sel_hi:[0,1]
	v_med3_f32 v5, v102, s70, v164
	v_med3_f32 v102, v98, s70, v164
	v_med3_f32 v103, v103, s70, v164
	v_mov_b32_e32 v98, v147
	v_cvt_pk_fp8_f32 v98, v5, v103
	v_med3_f32 v116, v116, s70, v164
	v_med3_f32 v117, v117, s70, v164
	v_pk_fma_f32 v[104:105], v[104:105], s[36:37], v[156:157] op_sel_hi:[1,0,1]
	v_pk_fma_f32 v[100:101], v[100:101], s[36:37], v[152:153] op_sel_hi:[1,0,1]
	v_cvt_pk_fp8_f32 v115, v116, v117 op_sel:[0,0,1]
	v_med3_f32 v116, v107, s70, v164
	v_mov_b32_e32 v107, v147
	v_pk_mul_f32 v[104:105], v[112:113], v[104:105] op_sel_hi:[0,1]
	v_pk_mul_f32 v[100:101], v[112:113], v[100:101] op_sel_hi:[0,1]
	v_med3_f32 v113, v99, s70, v164
	v_pk_fma_f32 v[94:95], v[94:95], s[36:37], v[150:151] op_sel_hi:[1,0,1]
	v_pk_fma_f32 v[90:91], v[90:91], s[36:37], v[6:7] op_sel_hi:[1,0,1]
	v_cvt_pk_fp8_f32 v107, v110, v116
	v_med3_f32 v104, v104, s70, v164
	v_med3_f32 v5, v105, s70, v164
	v_pk_mul_f32 v[94:95], v[112:113], v[94:95] op_sel_hi:[0,1]
	v_pk_mul_f32 v[90:91], v[112:113], v[90:91] op_sel_hi:[0,1]
	v_pk_fma_f32 v[108:109], v[108:109], s[36:37], v[2:3] op_sel_hi:[1,0,1]
	v_mov_b32_e32 v99, v147
	v_cvt_pk_fp8_f32 v98, v104, v5 op_sel:[0,0,1]
	v_med3_f32 v5, v94, s70, v164
	v_med3_f32 v94, v90, s70, v164
	v_med3_f32 v95, v95, s70, v164
	v_mov_b32_e32 v90, v147
	s_lshl_b32 s6, s50, 8
	ds_read_b128 v[124:127], v123
	v_pk_mul_f32 v[108:109], v[130:131], v[108:109] op_sel_hi:[0,1]
	v_cvt_pk_fp8_f32 v99, v102, v113
	v_cvt_pk_fp8_f32 v90, v5, v95
	s_or_b32 s6, s7, s6
	v_med3_f32 v108, v108, s70, v164
	v_med3_f32 v109, v109, s70, v164
	v_pk_fma_f32 v[96:97], v[96:97], s[36:37], v[8:9] op_sel_hi:[1,0,1]
	s_ashr_i32 s7, s6, 31
	v_lshl_add_u64 v[128:129], s[16:17], 0, v[128:129]
	v_cvt_pk_fp8_f32 v107, v108, v109 op_sel:[0,0,1]
	v_pk_mul_f32 v[96:97], v[112:113], v[96:97] op_sel_hi:[0,1]
	v_lshl_add_u64 v[128:129], v[128:129], 0, s[6:7]
	v_med3_f32 v100, v100, s70, v164
	v_med3_f32 v101, v101, s70, v164
	v_med3_f32 v96, v96, s70, v164
	v_med3_f32 v5, v97, s70, v164
	v_lshl_add_u64 v[108:109], v[128:129], 0, v[146:147]
	v_cvt_pk_fp8_f32 v99, v100, v101 op_sel:[0,0,1]
	v_med3_f32 v100, v91, s70, v164
	v_mov_b32_e32 v91, v147
	v_cvt_pk_fp8_f32 v90, v96, v5 op_sel:[0,0,1]
	v_mul_f32_e32 v96, 0x41000000, v168
	v_pk_fma_f32 v[78:79], v[78:79], s[36:37], v[158:159] op_sel_hi:[1,0,1]
	v_pk_fma_f32 v[74:75], v[74:75], s[36:37], v[154:155] op_sel_hi:[1,0,1]
	s_waitcnt lgkmcnt(0)
	global_store_dwordx4 v[108:109], v[124:127], off
	v_cvt_pk_fp8_f32 v91, v94, v100
	v_pk_fma_f32 v[80:81], v[80:81], s[36:37], v[156:157] op_sel_hi:[1,0,1]
	v_pk_mul_f32 v[78:79], v[96:97], v[78:79] op_sel_hi:[0,1]
	v_pk_fma_f32 v[76:77], v[76:77], s[36:37], v[152:153] op_sel_hi:[1,0,1]
	v_pk_mul_f32 v[74:75], v[96:97], v[74:75] op_sel_hi:[0,1]
	ds_write2_b64 v122, v[114:115], v[106:107] offset1:4
	v_or_b32_e32 v110, 16, v4
	v_pk_fma_f32 v[92:93], v[92:93], s[36:37], v[2:3] op_sel_hi:[1,0,1]
	v_pk_mul_f32 v[80:81], v[96:97], v[80:81] op_sel_hi:[0,1]
	v_pk_mul_f32 v[76:77], v[96:97], v[76:77] op_sel_hi:[0,1]
	v_med3_f32 v5, v78, s70, v164
	v_med3_f32 v78, v74, s70, v164
	v_med3_f32 v79, v79, s70, v164
	v_med3_f32 v97, v75, s70, v164
	v_mov_b32_e32 v74, v147
	v_mov_b32_e32 v75, v147
	ds_read_b128 v[106:109], v123
	v_ashrrev_i32_e32 v111, 31, v110
	v_pk_mul_f32 v[92:93], v[112:113], v[92:93] op_sel_hi:[0,1]
	v_cvt_pk_fp8_f32 v74, v5, v79
	v_cvt_pk_fp8_f32 v75, v78, v97
	v_lshlrev_b64 v[110:111], 10, v[110:111]
	v_med3_f32 v92, v92, s70, v164
	v_med3_f32 v93, v93, s70, v164
	v_lshl_add_u64 v[110:111], s[16:17], 0, v[110:111]
	v_cvt_pk_fp8_f32 v91, v92, v93 op_sel:[0,0,1]
	v_pk_fma_f32 v[62:63], v[62:63], s[36:37], v[150:151] op_sel_hi:[1,0,1]
	v_pk_fma_f32 v[58:59], v[58:59], s[36:37], v[6:7] op_sel_hi:[1,0,1]
	v_lshl_add_u64 v[110:111], v[110:111], 0, s[6:7]
	v_med3_f32 v80, v80, s70, v164
	v_med3_f32 v76, v76, s70, v164
	v_med3_f32 v5, v81, s70, v164
	v_med3_f32 v77, v77, s70, v164
	v_pk_mul_f32 v[62:63], v[96:97], v[62:63] op_sel_hi:[0,1]
	v_pk_mul_f32 v[58:59], v[96:97], v[58:59] op_sel_hi:[0,1]
	v_lshl_add_u64 v[92:93], v[110:111], 0, v[146:147]
	v_cvt_pk_fp8_f32 v74, v80, v5 op_sel:[0,0,1]
	v_cvt_pk_fp8_f32 v75, v76, v77 op_sel:[0,0,1]
	v_med3_f32 v5, v62, s70, v164
	v_med3_f32 v62, v58, s70, v164
	v_med3_f32 v63, v63, s70, v164
	v_med3_f32 v76, v59, s70, v164
	v_mov_b32_e32 v58, v147
	v_mov_b32_e32 v59, v147
	s_waitcnt lgkmcnt(0)
	global_store_dwordx4 v[92:93], v[106:109], off
	v_cvt_pk_fp8_f32 v58, v5, v63
	v_cvt_pk_fp8_f32 v59, v62, v76
	ds_write2_b64 v122, v[98:99], v[90:91] offset1:4
	v_or_b32_e32 v94, 32, v4
	v_pk_fma_f32 v[64:65], v[64:65], s[36:37], v[8:9] op_sel_hi:[1,0,1]
	v_pk_fma_f32 v[60:61], v[60:61], s[36:37], v[2:3] op_sel_hi:[1,0,1]
	ds_read_b128 v[90:93], v123
	v_ashrrev_i32_e32 v95, 31, v94
	v_pk_mul_f32 v[64:65], v[96:97], v[64:65] op_sel_hi:[0,1]
	v_pk_mul_f32 v[60:61], v[96:97], v[60:61] op_sel_hi:[0,1]
	v_lshlrev_b64 v[94:95], 10, v[94:95]
	v_med3_f32 v64, v64, s70, v164
	v_med3_f32 v60, v60, s70, v164
	v_med3_f32 v5, v65, s70, v164
	v_med3_f32 v61, v61, s70, v164
	v_lshl_add_u64 v[94:95], s[16:17], 0, v[94:95]
	v_cvt_pk_fp8_f32 v58, v64, v5 op_sel:[0,0,1]
	v_cvt_pk_fp8_f32 v59, v60, v61 op_sel:[0,0,1]
	v_lshl_add_u64 v[94:95], v[94:95], 0, s[6:7]
	v_lshl_add_u64 v[60:61], v[94:95], 0, v[146:147]
	s_waitcnt lgkmcnt(0)
	global_store_dwordx4 v[60:61], v[90:93], off
	ds_write2_b64 v122, v[74:75], v[58:59] offset1:4
	v_mul_f32_e32 v64, 0x41000000, v167
	v_pk_fma_f32 v[74:75], v[86:87], s[36:37], v[158:159] op_sel_hi:[1,0,1]
	v_pk_fma_f32 v[78:79], v[82:83], s[36:37], v[154:155] op_sel_hi:[1,0,1]
	v_pk_mul_f32 v[74:75], v[64:65], v[74:75] op_sel_hi:[0,1]
	v_pk_fma_f32 v[76:77], v[88:89], s[36:37], v[156:157] op_sel_hi:[1,0,1]
	v_pk_fma_f32 v[80:81], v[84:85], s[36:37], v[152:153] op_sel_hi:[1,0,1]
	v_pk_mul_f32 v[78:79], v[64:65], v[78:79] op_sel_hi:[0,1]
	v_med3_f32 v5, v74, s70, v164
	v_med3_f32 v75, v75, s70, v164
	v_mov_b32_e32 v74, v147
	v_pk_mul_f32 v[76:77], v[64:65], v[76:77] op_sel_hi:[0,1]
	v_pk_mul_f32 v[80:81], v[64:65], v[80:81] op_sel_hi:[0,1]
	v_med3_f32 v65, v78, s70, v164
	v_med3_f32 v78, v79, s70, v164
	v_cvt_pk_fp8_f32 v74, v5, v75
	v_mov_b32_e32 v75, v147
	v_cvt_pk_fp8_f32 v75, v65, v78
	v_med3_f32 v79, v80, s70, v164
	v_med3_f32 v65, v81, s70, v164
	v_pk_fma_f32 v[70:71], v[70:71], s[36:37], v[150:151] op_sel_hi:[1,0,1]
	v_pk_fma_f32 v[72:73], v[72:73], s[36:37], v[8:9] op_sel_hi:[1,0,1]
	v_pk_fma_f32 v[66:67], v[66:67], s[36:37], v[6:7] op_sel_hi:[1,0,1]
	v_pk_fma_f32 v[68:69], v[68:69], s[36:37], v[2:3] op_sel_hi:[1,0,1]
	v_med3_f32 v76, v76, s70, v164
	v_med3_f32 v5, v77, s70, v164
	v_cvt_pk_fp8_f32 v75, v79, v65 op_sel:[0,0,1]
	v_pk_mul_f32 v[72:73], v[64:65], v[72:73] op_sel_hi:[0,1]
	v_pk_mul_f32 v[70:71], v[64:65], v[70:71] op_sel_hi:[0,1]
	v_pk_mul_f32 v[68:69], v[64:65], v[68:69] op_sel_hi:[0,1]
	v_pk_mul_f32 v[64:65], v[64:65], v[66:67] op_sel_hi:[0,1]
	v_cvt_pk_fp8_f32 v74, v76, v5 op_sel:[0,0,1]
	v_med3_f32 v5, v70, s70, v164
	v_med3_f32 v66, v64, s70, v164
	v_med3_f32 v67, v71, s70, v164
	v_med3_f32 v70, v65, s70, v164
	v_mov_b32_e32 v64, v147
	v_mov_b32_e32 v65, v147
	v_cvt_pk_fp8_f32 v64, v5, v67
	v_cvt_pk_fp8_f32 v65, v66, v70
	v_or_b32_e32 v62, 48, v4
	ds_read_b128 v[58:61], v123
	v_ashrrev_i32_e32 v63, 31, v62
	v_lshlrev_b64 v[62:63], 10, v[62:63]
	v_med3_f32 v71, v72, s70, v164
	v_med3_f32 v68, v68, s70, v164
	v_med3_f32 v5, v73, s70, v164
	v_med3_f32 v66, v69, s70, v164
	v_lshl_add_u64 v[62:63], s[16:17], 0, v[62:63]
	v_cvt_pk_fp8_f32 v64, v71, v5 op_sel:[0,0,1]
	v_cvt_pk_fp8_f32 v65, v68, v66 op_sel:[0,0,1]
	v_lshl_add_u64 v[62:63], v[62:63], 0, s[6:7]
	v_lshl_add_u64 v[62:63], v[62:63], 0, v[146:147]
	s_waitcnt lgkmcnt(0)
	global_store_dwordx4 v[62:63], v[58:61], off
	ds_write2_b64 v122, v[74:75], v[64:65] offset1:4
	v_mul_f32_e32 v64, 0x41000000, v166
	v_pk_fma_f32 v[54:55], v[54:55], s[36:37], v[158:159] op_sel_hi:[1,0,1]
	v_pk_fma_f32 v[50:51], v[50:51], s[36:37], v[154:155] op_sel_hi:[1,0,1]
	v_pk_mul_f32 v[54:55], v[64:65], v[54:55] op_sel_hi:[0,1]
	v_pk_mul_f32 v[50:51], v[64:65], v[50:51] op_sel_hi:[0,1]
	v_med3_f32 v5, v54, s70, v164
	v_med3_f32 v54, v50, s70, v164
	v_med3_f32 v55, v55, s70, v164
	v_mov_b32_e32 v50, v147
	v_cvt_pk_fp8_f32 v50, v5, v55
	v_pk_fma_f32 v[56:57], v[56:57], s[36:37], v[156:157] op_sel_hi:[1,0,1]
	v_pk_fma_f32 v[52:53], v[52:53], s[36:37], v[152:153] op_sel_hi:[1,0,1]
	v_pk_mul_f32 v[56:57], v[64:65], v[56:57] op_sel_hi:[0,1]
	v_pk_mul_f32 v[52:53], v[64:65], v[52:53] op_sel_hi:[0,1]
	v_med3_f32 v65, v51, s70, v164
	v_pk_fma_f32 v[46:47], v[46:47], s[36:37], v[150:151] op_sel_hi:[1,0,1]
	v_pk_fma_f32 v[42:43], v[42:43], s[36:37], v[6:7] op_sel_hi:[1,0,1]
	v_med3_f32 v56, v56, s70, v164
	v_med3_f32 v5, v57, s70, v164
	v_pk_mul_f32 v[46:47], v[64:65], v[46:47] op_sel_hi:[0,1]
	v_pk_mul_f32 v[42:43], v[64:65], v[42:43] op_sel_hi:[0,1]
	v_cvt_pk_fp8_f32 v50, v56, v5 op_sel:[0,0,1]
	v_med3_f32 v5, v46, s70, v164
	v_med3_f32 v46, v42, s70, v164
	v_med3_f32 v47, v47, s70, v164
	v_mov_b32_e32 v42, v147
	v_cvt_pk_fp8_f32 v42, v5, v47
	v_pk_fma_f32 v[48:49], v[48:49], s[36:37], v[8:9] op_sel_hi:[1,0,1]
	v_mov_b32_e32 v51, v147
	v_pk_mul_f32 v[48:49], v[64:65], v[48:49] op_sel_hi:[0,1]
	v_med3_f32 v48, v48, s70, v164
	v_med3_f32 v5, v49, s70, v164
	v_cvt_pk_fp8_f32 v42, v48, v5 op_sel:[0,0,1]
	v_mul_f32_e32 v48, 0x41000000, v165
	v_pk_fma_f32 v[38:39], v[38:39], s[36:37], v[158:159] op_sel_hi:[1,0,1]
	v_pk_fma_f32 v[34:35], v[34:35], s[36:37], v[154:155] op_sel_hi:[1,0,1]
	v_cvt_pk_fp8_f32 v51, v54, v65
	v_pk_mul_f32 v[38:39], v[48:49], v[38:39] op_sel_hi:[0,1]
	v_pk_mul_f32 v[34:35], v[48:49], v[34:35] op_sel_hi:[0,1]
	v_med3_f32 v5, v38, s70, v164
	v_med3_f32 v38, v34, s70, v164
	v_med3_f32 v39, v39, s70, v164
	v_mov_b32_e32 v34, v147
	v_cvt_pk_fp8_f32 v34, v5, v39
	v_med3_f32 v52, v52, s70, v164
	v_med3_f32 v53, v53, s70, v164
	v_pk_fma_f32 v[40:41], v[40:41], s[36:37], v[156:157] op_sel_hi:[1,0,1]
	v_pk_fma_f32 v[36:37], v[36:37], s[36:37], v[152:153] op_sel_hi:[1,0,1]
	v_cvt_pk_fp8_f32 v51, v52, v53 op_sel:[0,0,1]
	v_med3_f32 v52, v43, s70, v164
	v_mov_b32_e32 v43, v147
	v_pk_mul_f32 v[40:41], v[48:49], v[40:41] op_sel_hi:[0,1]
	v_pk_mul_f32 v[36:37], v[48:49], v[36:37] op_sel_hi:[0,1]
	v_med3_f32 v49, v35, s70, v164
	v_pk_fma_f32 v[30:31], v[30:31], s[36:37], v[150:151] op_sel_hi:[1,0,1]
	v_pk_fma_f32 v[26:27], v[26:27], s[36:37], v[6:7] op_sel_hi:[1,0,1]
	v_cvt_pk_fp8_f32 v43, v46, v52
	v_med3_f32 v40, v40, s70, v164
	v_med3_f32 v5, v41, s70, v164
	v_pk_mul_f32 v[30:31], v[48:49], v[30:31] op_sel_hi:[0,1]
	v_pk_mul_f32 v[26:27], v[48:49], v[26:27] op_sel_hi:[0,1]
	v_add_u32_e32 v62, 0x80, v4
	v_pk_fma_f32 v[44:45], v[44:45], s[36:37], v[2:3] op_sel_hi:[1,0,1]
	v_mov_b32_e32 v35, v147
	v_cvt_pk_fp8_f32 v34, v40, v5 op_sel:[0,0,1]
	v_med3_f32 v5, v30, s70, v164
	v_med3_f32 v30, v26, s70, v164
	v_med3_f32 v31, v31, s70, v164
	v_mov_b32_e32 v26, v147
	ds_read_b128 v[58:61], v123
	v_ashrrev_i32_e32 v63, 31, v62
	v_pk_mul_f32 v[44:45], v[64:65], v[44:45] op_sel_hi:[0,1]
	v_cvt_pk_fp8_f32 v35, v38, v49
	v_cvt_pk_fp8_f32 v26, v5, v31
	v_lshlrev_b64 v[62:63], 10, v[62:63]
	v_med3_f32 v44, v44, s70, v164
	v_med3_f32 v45, v45, s70, v164
	v_pk_fma_f32 v[32:33], v[32:33], s[36:37], v[8:9] op_sel_hi:[1,0,1]
	v_lshl_add_u64 v[62:63], s[16:17], 0, v[62:63]
	v_cvt_pk_fp8_f32 v43, v44, v45 op_sel:[0,0,1]
	v_pk_mul_f32 v[32:33], v[48:49], v[32:33] op_sel_hi:[0,1]
	v_lshl_add_u64 v[62:63], v[62:63], 0, s[6:7]
	v_med3_f32 v36, v36, s70, v164
	v_med3_f32 v37, v37, s70, v164
	v_med3_f32 v32, v32, s70, v164
	v_med3_f32 v5, v33, s70, v164
	v_lshl_add_u64 v[44:45], v[62:63], 0, v[146:147]
	v_cvt_pk_fp8_f32 v35, v36, v37 op_sel:[0,0,1]
	v_med3_f32 v36, v27, s70, v164
	v_mov_b32_e32 v27, v147
	v_cvt_pk_fp8_f32 v26, v32, v5 op_sel:[0,0,1]
	v_mul_f32_e32 v32, 0x41000000, v1
	v_pk_fma_f32 v[22:23], v[22:23], s[36:37], v[158:159] op_sel_hi:[1,0,1]
	v_pk_fma_f32 v[18:19], v[18:19], s[36:37], v[154:155] op_sel_hi:[1,0,1]
	s_waitcnt lgkmcnt(0)
	global_store_dwordx4 v[44:45], v[58:61], off
	v_cvt_pk_fp8_f32 v27, v30, v36
	v_pk_mul_f32 v[22:23], v[32:33], v[22:23] op_sel_hi:[0,1]
	v_pk_mul_f32 v[18:19], v[32:33], v[18:19] op_sel_hi:[0,1]
	ds_write2_b64 v122, v[50:51], v[42:43] offset1:4
	v_add_u32_e32 v46, 0x90, v4
	v_pk_fma_f32 v[28:29], v[28:29], s[36:37], v[2:3] op_sel_hi:[1,0,1]
	v_med3_f32 v1, v22, s70, v164
	v_med3_f32 v5, v18, s70, v164
	v_med3_f32 v22, v23, s70, v164
	v_med3_f32 v23, v19, s70, v164
	v_mov_b32_e32 v18, v147
	v_mov_b32_e32 v19, v147
	ds_read_b128 v[42:45], v123
	v_ashrrev_i32_e32 v47, 31, v46
	v_pk_mul_f32 v[28:29], v[48:49], v[28:29] op_sel_hi:[0,1]
	v_cvt_pk_fp8_f32 v18, v1, v22
	v_cvt_pk_fp8_f32 v19, v5, v23
	v_lshlrev_b64 v[46:47], 10, v[46:47]
	v_med3_f32 v28, v28, s70, v164
	v_med3_f32 v29, v29, s70, v164
	v_pk_fma_f32 v[24:25], v[24:25], s[36:37], v[156:157] op_sel_hi:[1,0,1]
	v_pk_fma_f32 v[20:21], v[20:21], s[36:37], v[152:153] op_sel_hi:[1,0,1]
	v_lshl_add_u64 v[46:47], s[16:17], 0, v[46:47]
	v_cvt_pk_fp8_f32 v27, v28, v29 op_sel:[0,0,1]
	v_pk_mul_f32 v[24:25], v[32:33], v[24:25] op_sel_hi:[0,1]
	v_pk_mul_f32 v[20:21], v[32:33], v[20:21] op_sel_hi:[0,1]
	v_pk_fma_f32 v[14:15], v[14:15], s[36:37], v[150:151] op_sel_hi:[1,0,1]
	v_pk_fma_f32 v[6:7], v[10:11], s[36:37], v[6:7] op_sel_hi:[1,0,1]
	v_lshl_add_u64 v[46:47], v[46:47], 0, s[6:7]
	v_med3_f32 v24, v24, s70, v164
	v_med3_f32 v20, v20, s70, v164
	v_med3_f32 v1, v25, s70, v164
	v_med3_f32 v5, v21, s70, v164
	v_pk_mul_f32 v[14:15], v[32:33], v[14:15] op_sel_hi:[0,1]
	v_pk_mul_f32 v[6:7], v[32:33], v[6:7] op_sel_hi:[0,1]
	v_lshl_add_u64 v[28:29], v[46:47], 0, v[146:147]
	v_cvt_pk_fp8_f32 v18, v24, v1 op_sel:[0,0,1]
	v_cvt_pk_fp8_f32 v19, v20, v5 op_sel:[0,0,1]
	v_med3_f32 v1, v14, s70, v164
	v_med3_f32 v5, v6, s70, v164
	v_med3_f32 v10, v15, s70, v164
	v_med3_f32 v11, v7, s70, v164
	v_mov_b32_e32 v6, v147
	v_mov_b32_e32 v7, v147
	s_waitcnt lgkmcnt(0)
	global_store_dwordx4 v[28:29], v[42:45], off
	v_cvt_pk_fp8_f32 v6, v1, v10
	v_cvt_pk_fp8_f32 v7, v5, v11
	ds_write2_b64 v122, v[34:35], v[26:27] offset1:4
	v_add_u32_e32 v30, 0xa0, v4
	v_pk_fma_f32 v[8:9], v[16:17], s[36:37], v[8:9] op_sel_hi:[1,0,1]
	v_pk_fma_f32 v[2:3], v[12:13], s[36:37], v[2:3] op_sel_hi:[1,0,1]
	ds_read_b128 v[26:29], v123
	v_ashrrev_i32_e32 v31, 31, v30
	v_pk_mul_f32 v[8:9], v[32:33], v[8:9] op_sel_hi:[0,1]
	v_pk_mul_f32 v[2:3], v[32:33], v[2:3] op_sel_hi:[0,1]
	v_lshlrev_b64 v[30:31], 10, v[30:31]
	v_med3_f32 v8, v8, s70, v164
	v_med3_f32 v2, v2, s70, v164
	v_med3_f32 v1, v9, s70, v164
	v_med3_f32 v3, v3, s70, v164
	v_lshl_add_u64 v[30:31], s[16:17], 0, v[30:31]
	v_cvt_pk_fp8_f32 v6, v8, v1 op_sel:[0,0,1]
	v_cvt_pk_fp8_f32 v7, v2, v3 op_sel:[0,0,1]
	v_lshl_add_u64 v[30:31], v[30:31], 0, s[6:7]
	v_lshl_add_u64 v[2:3], v[30:31], 0, v[146:147]
	s_waitcnt lgkmcnt(0)
	global_store_dwordx4 v[2:3], v[26:29], off
	ds_write2_b64 v122, v[18:19], v[6:7] offset1:4
	v_add_u32_e32 v2, 0xb0, v4
	ds_read_b128 v[6:9], v123
	v_ashrrev_i32_e32 v3, 31, v2
	v_lshlrev_b64 v[2:3], 10, v[2:3]
	v_lshl_add_u64 v[2:3], s[16:17], 0, v[2:3]
	v_lshl_add_u64 v[2:3], v[2:3], 0, s[6:7]
	v_lshl_add_u64 v[2:3], v[2:3], 0, v[146:147]
	s_waitcnt lgkmcnt(0)
	global_store_dwordx4 v[2:3], v[6:9], off
	s_and_b64 vcc, exec, s[8:9]
	s_mov_b64 s[6:7], -1
	s_cbranch_vccnz .LBB0_1616
	v_mov_b32_e32 v12, v0
	s_lshl_b32 s7, s40, 8
	v_readfirstlane_b32 s6, v12
	s_and_b32 s8, s6, 0xc0
	s_ashr_i32 s6, s6, 2
	s_andn2_b32 s6, s6, 63
	s_add_i32 s6, s6, s7
	v_and_or_b32 v2, v12, 15, s6
	v_lshlrev_b32_e32 v4, 2, v2
	s_lshl_b64 s[6:7], s[42:43], 11
	s_add_u32 s9, s56, s6
	s_addc_u32 s39, s57, s7
	s_lshl_b32 s6, s38, 8
	global_load_dword v146, v4, s[12:13] offset:0
	global_load_dword v170, v4, s[12:13] offset:64
	global_load_dword v169, v4, s[12:13] offset:128
	global_load_dword v168, v4, s[12:13] offset:192
	global_load_dword v167, v4, s[12:13] offset:512
	global_load_dword v166, v4, s[12:13] offset:576
	global_load_dword v165, v4, s[12:13] offset:640
	global_load_dword v1, v4, s[12:13] offset:704
	s_ashr_i32 s7, s6, 31
	s_lshl_b64 s[6:7], s[6:7], 1
	s_add_u32 s6, s9, s6
	s_addc_u32 s7, s39, s7
	s_lshl_b32 s8, s8, 1
	s_add_u32 s6, s6, s8
	s_addc_u32 s7, s7, 0
	v_and_b32_e32 v2, 48, v12
	global_load_dwordx4 v[6:9], v2, s[6:7]
	s_nop 0
	global_load_dwordx4 v[2:5], v2, s[6:7] offset:64
	s_andn2_b64 vcc, exec, s[14:15]
	s_cbranch_vccnz .LBB0_1615
	s_barrier
	s_branch .LBB0_1615

.LBB0_3348:
	s_mov_b32 s82, 0xc2700000
	v_mov_b32_e32 v190, 0x41898193
	v_lshlrev_b32_e32 v160, 16, v46
	v_and_b32_e32 v161, 0xffff0000, v46
	v_lshlrev_b32_e32 v156, 16, v42
	v_and_b32_e32 v157, 0xffff0000, v42
	v_mul_f32_e32 v42, 0x3d800000, v179
	v_lshlrev_b32_e32 v154, 16, v47
	v_and_b32_e32 v155, 0xffff0000, v47
	v_lshlrev_b32_e32 v46, 16, v44
	v_and_b32_e32 v47, 0xffff0000, v44
	v_lshlrev_b32_e32 v150, 16, v45
	v_and_b32_e32 v151, 0xffff0000, v45
	v_pk_fma_f32 v[44:45], v[42:43], v[130:131], v[160:161] op_sel_hi:[0,1,1]
	v_med3_f32 v44, v44, s82, v190
	v_med3_f32 v45, v45, s82, v190
	v_exp_f32_e64 v130, -v44
	v_exp_f32_e64 v131, -v45
	v_pk_fma_f32 v[132:133], v[42:43], v[132:133], v[154:155] op_sel_hi:[0,1,1]
	v_med3_f32 v132, v132, s82, v190
	v_med3_f32 v133, v133, s82, v190
	v_pk_add_f32 v[130:131], v[130:131], 1.0 op_sel_hi:[1,0]
	v_exp_f32_e64 v188, -v132
	v_exp_f32_e64 v189, -v133
	v_lshlrev_b32_e32 v152, 16, v48
	v_and_b32_e32 v153, 0xffff0000, v48
	v_pk_add_f32 v[188:189], v[188:189], 1.0 op_sel_hi:[1,0]
	v_pk_fma_f32 v[122:123], v[42:43], v[122:123], v[152:153] op_sel_hi:[0,1,1]
	v_pk_mul_f32 v[184:185], v[130:131], v[188:189]
	v_rcp_f32_e32 v184, v184
	v_rcp_f32_e32 v185, v185
	s_nop 0
	v_pk_mul_f32 v[186:187], v[184:185], v[188:189]
	v_pk_mul_f32 v[188:189], v[184:185], v[130:131]
	v_pk_mul_f32 v[44:45], v[44:45], v[186:187]
	v_med3_f32 v122, v122, s82, v190
	v_med3_f32 v123, v123, s82, v190
	v_lshlrev_b32_e32 v48, 16, v49
	v_pk_mul_f32 v[130:131], v[132:133], v[188:189]
	v_exp_f32_e64 v132, -v122
	v_exp_f32_e64 v133, -v123
	v_and_b32_e32 v49, 0xffff0000, v49
	v_pk_fma_f32 v[124:125], v[42:43], v[124:125], v[48:49] op_sel_hi:[0,1,1]
	v_lshlrev_b32_e32 v158, 16, v43
	v_and_b32_e32 v159, 0xffff0000, v43
	v_med3_f32 v124, v124, s82, v190
	v_med3_f32 v125, v125, s82, v190
	v_pk_fma_f32 v[136:137], v[42:43], v[136:137], v[158:159] op_sel_hi:[0,1,1]
	v_pk_fma_f32 v[134:135], v[42:43], v[134:135], v[156:157] op_sel_hi:[0,1,1]
	v_pk_fma_f32 v[128:129], v[42:43], v[128:129], v[150:151] op_sel_hi:[0,1,1]
	v_pk_add_f32 v[132:133], v[132:133], 1.0 op_sel_hi:[1,0]
	v_pk_fma_f32 v[42:43], v[42:43], v[126:127], v[46:47] op_sel_hi:[0,1,1]
	v_exp_f32_e64 v188, -v124
	v_exp_f32_e64 v189, -v125
	v_med3_f32 v42, v42, s81, v170
	v_pk_add_f32 v[188:189], v[188:189], 1.0 op_sel_hi:[1,0]
	v_med3_f32 v43, v43, s81, v170
	v_pk_mul_f32 v[184:185], v[132:133], v[188:189]
	v_rcp_f32_e32 v184, v184
	v_rcp_f32_e32 v185, v185
	s_nop 0
	v_pk_mul_f32 v[186:187], v[184:185], v[188:189]
	v_pk_mul_f32 v[188:189], v[184:185], v[132:133]
	v_pk_mul_f32 v[122:123], v[122:123], v[186:187]
	v_pk_mul_f32 v[42:43], v[122:123], v[42:43]
	v_med3_f32 v123, v129, s81, v170
	v_mov_b32_e32 v129, 0
	v_cvt_pk_fp8_f32 v129, v42, v43
	v_med3_f32 v122, v128, s81, v170
	v_pk_mul_f32 v[42:43], v[124:125], v[188:189]
	v_med3_f32 v134, v134, s81, v170
	v_med3_f32 v135, v135, s81, v170
	v_pk_mul_f32 v[42:43], v[42:43], v[122:123]
	v_pk_mul_f32 v[44:45], v[44:45], v[134:135]
	v_mov_b32_e32 v128, 0
	v_cvt_pk_fp8_f32 v129, v42, v43 op_sel:[0,0,1]
	v_mul_f32_e32 v42, 0x3d800000, v178
	v_cvt_pk_fp8_f32 v128, v44, v45
	v_pk_fma_f32 v[44:45], v[42:43], v[114:115], v[160:161] op_sel_hi:[0,1,1]
	v_med3_f32 v44, v44, s82, v190
	v_med3_f32 v45, v45, s82, v190
	v_exp_f32_e64 v114, -v44
	v_exp_f32_e64 v115, -v45
	v_pk_fma_f32 v[116:117], v[42:43], v[116:117], v[154:155] op_sel_hi:[0,1,1]
	v_med3_f32 v116, v116, s82, v190
	v_med3_f32 v117, v117, s82, v190
	v_pk_add_f32 v[114:115], v[114:115], 1.0 op_sel_hi:[1,0]
	v_exp_f32_e64 v188, -v116
	v_exp_f32_e64 v189, -v117
	v_pk_fma_f32 v[106:107], v[42:43], v[106:107], v[152:153] op_sel_hi:[0,1,1]
	v_med3_f32 v106, v106, s82, v190
	v_pk_add_f32 v[188:189], v[188:189], 1.0 op_sel_hi:[1,0]
	v_med3_f32 v107, v107, s82, v190
	v_pk_mul_f32 v[184:185], v[114:115], v[188:189]
	v_rcp_f32_e32 v184, v184
	v_rcp_f32_e32 v185, v185
	s_nop 0
	v_pk_mul_f32 v[186:187], v[184:185], v[188:189]
	v_pk_mul_f32 v[188:189], v[184:185], v[114:115]
	v_pk_mul_f32 v[44:45], v[44:45], v[186:187]
	v_pk_fma_f32 v[108:109], v[42:43], v[108:109], v[48:49] op_sel_hi:[0,1,1]
	v_med3_f32 v108, v108, s82, v190
	v_med3_f32 v109, v109, s82, v190
	v_pk_mul_f32 v[114:115], v[116:117], v[188:189]
	v_exp_f32_e64 v116, -v106
	v_exp_f32_e64 v117, -v107
	v_pk_fma_f32 v[120:121], v[42:43], v[120:121], v[158:159] op_sel_hi:[0,1,1]
	v_pk_fma_f32 v[118:119], v[42:43], v[118:119], v[156:157] op_sel_hi:[0,1,1]
	v_pk_fma_f32 v[112:113], v[42:43], v[112:113], v[150:151] op_sel_hi:[0,1,1]
	v_pk_add_f32 v[116:117], v[116:117], 1.0 op_sel_hi:[1,0]
	v_pk_fma_f32 v[42:43], v[42:43], v[110:111], v[46:47] op_sel_hi:[0,1,1]
	v_exp_f32_e64 v188, -v108
	v_exp_f32_e64 v189, -v109
	v_med3_f32 v118, v118, s81, v170
	v_pk_add_f32 v[188:189], v[188:189], 1.0 op_sel_hi:[1,0]
	v_med3_f32 v119, v119, s81, v170
	v_med3_f32 v42, v42, s81, v170
	v_med3_f32 v43, v43, s81, v170
	v_pk_mul_f32 v[184:185], v[116:117], v[188:189]
	v_rcp_f32_e32 v184, v184
	v_rcp_f32_e32 v185, v185
	s_nop 0
	v_pk_mul_f32 v[186:187], v[184:185], v[188:189]
	v_pk_mul_f32 v[188:189], v[184:185], v[116:117]
	v_pk_mul_f32 v[106:107], v[106:107], v[186:187]
	v_pk_mul_f32 v[44:45], v[44:45], v[118:119]
	v_pk_mul_f32 v[42:43], v[106:107], v[42:43]
	v_med3_f32 v106, v112, s81, v170
	v_med3_f32 v107, v113, s81, v170
	v_mov_b32_e32 v112, 0
	v_mov_b32_e32 v113, 0
	v_mov_b32_e32 v142, v0
	v_cvt_pk_fp8_f32 v112, v44, v45
	v_cvt_pk_fp8_f32 v113, v42, v43
	v_med3_f32 v134, v136, s81, v170
	v_readfirstlane_b32 s65, v142
	v_med3_f32 v135, v137, s81, v170
	s_ashr_i32 s10, s65, 6
	v_pk_mul_f32 v[130:131], v[130:131], v[134:135]
	v_med3_f32 v118, v120, s81, v170
	v_med3_f32 v119, v121, s81, v170
	v_pk_mul_f32 v[42:43], v[108:109], v[188:189]
	s_mul_i32 s11, s10, 0xb00
	v_cvt_pk_fp8_f32 v128, v130, v131 op_sel:[0,0,1]
	v_pk_mul_f32 v[114:115], v[114:115], v[118:119]
	v_pk_mul_f32 v[42:43], v[42:43], v[106:107]
	s_add_i32 s67, s11, 0
	v_and_b32_e32 v147, 15, v142
	v_lshrrev_b32_e32 v125, 1, v142
	v_cvt_pk_fp8_f32 v112, v114, v115 op_sel:[0,0,1]
	v_cvt_pk_fp8_f32 v113, v42, v43 op_sel:[0,0,1]
	s_add_i32 s67, s67, 0x20000
	v_mul_u32_u24_e32 v124, 48, v147
	v_and_b32_e32 v42, 24, v125
	v_add3_u32 v108, s67, v124, v42
	ds_write_b64 v108, v[128:129]
	ds_write_b64 v108, v[112:113] offset:768
	v_mul_f32_e32 v112, 0x3d800000, v177
	v_pk_fma_f32 v[98:99], v[112:113], v[98:99], v[160:161] op_sel_hi:[0,1,1]
	v_med3_f32 v98, v98, s82, v190
	v_med3_f32 v99, v99, s82, v190
	v_exp_f32_e64 v114, -v98
	v_exp_f32_e64 v115, -v99
	v_pk_fma_f32 v[100:101], v[112:113], v[100:101], v[154:155] op_sel_hi:[0,1,1]
	v_med3_f32 v100, v100, s82, v190
	v_med3_f32 v101, v101, s82, v190
	v_pk_add_f32 v[114:115], v[114:115], 1.0 op_sel_hi:[1,0]
	v_exp_f32_e64 v188, -v100
	v_exp_f32_e64 v189, -v101
	v_pk_fma_f32 v[102:103], v[112:113], v[102:103], v[156:157] op_sel_hi:[0,1,1]
	v_pk_fma_f32 v[90:91], v[112:113], v[90:91], v[152:153] op_sel_hi:[0,1,1]
	v_pk_add_f32 v[188:189], v[188:189], 1.0 op_sel_hi:[1,0]
	v_pk_fma_f32 v[104:105], v[112:113], v[104:105], v[158:159] op_sel_hi:[0,1,1]
	v_med3_f32 v102, v102, s81, v170
	v_med3_f32 v103, v103, s81, v170
	v_pk_mul_f32 v[184:185], v[114:115], v[188:189]
	v_rcp_f32_e32 v184, v184
	v_rcp_f32_e32 v185, v185
	s_nop 0
	v_pk_mul_f32 v[186:187], v[184:185], v[188:189]
	v_pk_mul_f32 v[188:189], v[184:185], v[114:115]
	v_pk_mul_f32 v[98:99], v[98:99], v[186:187]
	v_med3_f32 v90, v90, s82, v190
	v_med3_f32 v91, v91, s82, v190
	v_pk_mul_f32 v[98:99], v[98:99], v[102:103]
	v_med3_f32 v102, v104, s81, v170
	v_med3_f32 v103, v105, s81, v170
	v_exp_f32_e64 v104, -v90
	v_exp_f32_e64 v105, -v91
	v_pk_mul_f32 v[100:101], v[100:101], v[188:189]
	v_pk_fma_f32 v[92:93], v[112:113], v[92:93], v[48:49] op_sel_hi:[0,1,1]
	v_pk_mul_f32 v[100:101], v[100:101], v[102:103]
	v_pk_add_f32 v[102:103], v[104:105], 1.0 op_sel_hi:[1,0]
	v_med3_f32 v92, v92, s82, v190
	v_rcp_f32_e32 v102, v102
	v_rcp_f32_e32 v103, v103
	v_med3_f32 v93, v93, s82, v190
	v_pk_fma_f32 v[94:95], v[112:113], v[94:95], v[46:47] op_sel_hi:[0,1,1]
	v_pk_fma_f32 v[96:97], v[112:113], v[96:97], v[150:151] op_sel_hi:[0,1,1]
	v_pk_mul_f32 v[90:91], v[90:91], v[102:103]
	v_exp_f32_e64 v102, -v92
	v_exp_f32_e64 v103, -v93
	v_med3_f32 v94, v94, s81, v170
	v_med3_f32 v95, v95, s81, v170
	v_pk_mul_f32 v[90:91], v[90:91], v[94:95]
	v_med3_f32 v94, v96, s81, v170
	v_med3_f32 v95, v97, s81, v170
	v_pk_add_f32 v[96:97], v[102:103], 1.0 op_sel_hi:[1,0]
	v_mov_b32_e32 v103, v143
	v_rcp_f32_e32 v96, v96
	v_rcp_f32_e32 v97, v97
	v_cvt_pk_fp8_f32 v103, v90, v91
	v_mov_b32_e32 v102, v143
	v_bfe_u32 v106, v142, 1, 5
	v_pk_mul_f32 v[90:91], v[92:93], v[96:97]
	v_lshlrev_b32_e32 v43, 4, v142
	v_pk_mul_f32 v[90:91], v[90:91], v[94:95]
	s_ashr_i32 s65, s65, 2
	v_cvt_pk_fp8_f32 v103, v90, v91 op_sel:[0,0,1]
	v_mul_f32_e32 v90, 0x3d800000, v176
	v_pk_fma_f32 v[82:83], v[90:91], v[82:83], v[160:161] op_sel_hi:[0,1,1]
	v_med3_f32 v82, v82, s82, v190
	v_med3_f32 v83, v83, s82, v190
	v_exp_f32_e64 v92, -v82
	v_exp_f32_e64 v93, -v83
	v_pk_fma_f32 v[84:85], v[90:91], v[84:85], v[154:155] op_sel_hi:[0,1,1]
	v_med3_f32 v84, v84, s82, v190
	v_med3_f32 v85, v85, s82, v190
	v_pk_add_f32 v[92:93], v[92:93], 1.0 op_sel_hi:[1,0]
	v_exp_f32_e64 v188, -v84
	v_exp_f32_e64 v189, -v85
	v_pk_fma_f32 v[86:87], v[90:91], v[86:87], v[156:157] op_sel_hi:[0,1,1]
	v_pk_fma_f32 v[66:67], v[90:91], v[66:67], v[152:153] op_sel_hi:[0,1,1]
	v_pk_add_f32 v[188:189], v[188:189], 1.0 op_sel_hi:[1,0]
	v_pk_fma_f32 v[88:89], v[90:91], v[88:89], v[158:159] op_sel_hi:[0,1,1]
	v_med3_f32 v86, v86, s81, v170
	v_med3_f32 v87, v87, s81, v170
	v_pk_mul_f32 v[184:185], v[92:93], v[188:189]
	v_rcp_f32_e32 v184, v184
	v_rcp_f32_e32 v185, v185
	s_nop 0
	v_pk_mul_f32 v[186:187], v[184:185], v[188:189]
	v_pk_mul_f32 v[188:189], v[184:185], v[92:93]
	v_pk_mul_f32 v[82:83], v[82:83], v[186:187]
	v_med3_f32 v66, v66, s82, v190
	v_med3_f32 v67, v67, s82, v190
	v_pk_mul_f32 v[82:83], v[82:83], v[86:87]
	v_med3_f32 v86, v88, s81, v170
	v_med3_f32 v87, v89, s81, v170
	v_exp_f32_e64 v88, -v66
	v_exp_f32_e64 v89, -v67
	v_pk_mul_f32 v[84:85], v[84:85], v[188:189]
	v_pk_fma_f32 v[68:69], v[90:91], v[68:69], v[48:49] op_sel_hi:[0,1,1]
	v_pk_mul_f32 v[84:85], v[84:85], v[86:87]
	v_pk_add_f32 v[86:87], v[88:89], 1.0 op_sel_hi:[1,0]
	v_med3_f32 v68, v68, s82, v190
	v_rcp_f32_e32 v86, v86
	v_rcp_f32_e32 v87, v87
	v_med3_f32 v69, v69, s82, v190
	v_pk_fma_f32 v[74:75], v[90:91], v[74:75], v[46:47] op_sel_hi:[0,1,1]
	v_pk_fma_f32 v[76:77], v[90:91], v[76:77], v[150:151] op_sel_hi:[0,1,1]
	v_pk_mul_f32 v[66:67], v[66:67], v[86:87]
	v_exp_f32_e64 v86, -v68
	v_exp_f32_e64 v87, -v69
	v_med3_f32 v74, v74, s81, v170
	v_med3_f32 v75, v75, s81, v170
	v_pk_mul_f32 v[66:67], v[66:67], v[74:75]
	v_med3_f32 v74, v76, s81, v170
	v_med3_f32 v75, v77, s81, v170
	v_pk_add_f32 v[76:77], v[86:87], 1.0 op_sel_hi:[1,0]
	v_mov_b32_e32 v87, v143
	v_rcp_f32_e32 v76, v76
	v_rcp_f32_e32 v77, v77
	v_cvt_pk_fp8_f32 v87, v66, v67
	v_cvt_pk_fp8_f32 v102, v98, v99
	v_mov_b32_e32 v86, v143
	v_pk_mul_f32 v[66:67], v[68:69], v[76:77]
	v_mul_f32_e32 v68, 0x3d800000, v175
	v_pk_fma_f32 v[70:71], v[68:69], v[70:71], v[160:161] op_sel_hi:[0,1,1]
	v_med3_f32 v70, v70, s82, v190
	v_med3_f32 v71, v71, s82, v190
	v_pk_mul_f32 v[66:67], v[66:67], v[74:75]
	v_exp_f32_e64 v74, -v70
	v_exp_f32_e64 v75, -v71
	v_pk_fma_f32 v[72:73], v[68:69], v[72:73], v[154:155] op_sel_hi:[0,1,1]
	v_med3_f32 v72, v72, s82, v190
	v_med3_f32 v73, v73, s82, v190
	v_pk_add_f32 v[74:75], v[74:75], 1.0 op_sel_hi:[1,0]
	v_pk_fma_f32 v[76:77], v[68:69], v[80:81], v[158:159] op_sel_hi:[0,1,1]
	v_exp_f32_e64 v188, -v72
	v_exp_f32_e64 v189, -v73
	v_pk_fma_f32 v[58:59], v[68:69], v[58:59], v[152:153] op_sel_hi:[0,1,1]
	v_med3_f32 v58, v58, s82, v190
	v_pk_add_f32 v[188:189], v[188:189], 1.0 op_sel_hi:[1,0]
	v_med3_f32 v59, v59, s82, v190
	v_pk_mul_f32 v[184:185], v[74:75], v[188:189]
	v_rcp_f32_e32 v184, v184
	v_rcp_f32_e32 v185, v185
	s_nop 0
	v_pk_mul_f32 v[186:187], v[184:185], v[188:189]
	v_pk_mul_f32 v[188:189], v[184:185], v[74:75]
	v_pk_mul_f32 v[70:71], v[70:71], v[186:187]
	v_pk_fma_f32 v[60:61], v[68:69], v[60:61], v[48:49] op_sel_hi:[0,1,1]
	v_med3_f32 v60, v60, s82, v190
	v_med3_f32 v61, v61, s82, v190
	v_pk_mul_f32 v[72:73], v[72:73], v[188:189]
	v_exp_f32_e64 v74, -v58
	v_exp_f32_e64 v75, -v59
	v_pk_fma_f32 v[78:79], v[68:69], v[78:79], v[156:157] op_sel_hi:[0,1,1]
	v_pk_fma_f32 v[64:65], v[68:69], v[64:65], v[150:151] op_sel_hi:[0,1,1]
	v_pk_fma_f32 v[62:63], v[68:69], v[62:63], v[46:47] op_sel_hi:[0,1,1]
	v_pk_add_f32 v[74:75], v[74:75], 1.0 op_sel_hi:[1,0]
	v_exp_f32_e64 v188, -v60
	v_exp_f32_e64 v189, -v61
	v_med3_f32 v62, v62, s81, v170
	v_med3_f32 v63, v63, s81, v170
	v_mul_u32_u24_e32 v42, 48, v106
	v_pk_mul_f32 v[58:59], v[58:59], v[62:63]
	v_med3_f32 v62, v64, s81, v170
	v_med3_f32 v63, v65, s81, v170
	v_pk_add_f32 v[188:189], v[188:189], 1.0 op_sel_hi:[1,0]
	v_mov_b32_e32 v69, v143
	v_pk_mul_f32 v[184:185], v[74:75], v[188:189]
	v_rcp_f32_e32 v184, v184
	v_rcp_f32_e32 v185, v185
	s_nop 0
	v_pk_mul_f32 v[186:187], v[184:185], v[188:189]
	v_pk_mul_f32 v[188:189], v[184:185], v[74:75]
	v_pk_mul_f32 v[58:59], v[58:59], v[186:187]
	v_cvt_pk_fp8_f32 v69, v58, v59
	v_and_b32_e32 v142, 16, v43
	s_andn2_b32 s65, s65, 63
	v_pk_mul_f32 v[58:59], v[60:61], v[188:189]
	v_lshl_or_b32 v106, s74, 8, v106
	v_pk_mul_f32 v[58:59], v[58:59], v[62:63]
	v_cvt_pk_fp8_f32 v86, v82, v83
	v_cvt_pk_fp8_f32 v69, v58, v59 op_sel:[0,0,1]
	v_mul_f32_e32 v58, 0x3d800000, v174
	v_pk_fma_f32 v[50:51], v[58:59], v[50:51], v[160:161] op_sel_hi:[0,1,1]
	v_med3_f32 v50, v50, s82, v190
	v_med3_f32 v51, v51, s82, v190
	v_exp_f32_e64 v60, -v50
	v_exp_f32_e64 v61, -v51
	v_pk_fma_f32 v[52:53], v[58:59], v[52:53], v[154:155] op_sel_hi:[0,1,1]
	v_med3_f32 v52, v52, s82, v190
	v_med3_f32 v53, v53, s82, v190
	v_pk_add_f32 v[60:61], v[60:61], 1.0 op_sel_hi:[1,0]
	v_exp_f32_e64 v188, -v52
	v_exp_f32_e64 v189, -v53
	v_pk_fma_f32 v[54:55], v[58:59], v[54:55], v[156:157] op_sel_hi:[0,1,1]
	v_pk_fma_f32 v[34:35], v[58:59], v[34:35], v[152:153] op_sel_hi:[0,1,1]
	v_pk_add_f32 v[188:189], v[188:189], 1.0 op_sel_hi:[1,0]
	v_pk_fma_f32 v[56:57], v[58:59], v[56:57], v[158:159] op_sel_hi:[0,1,1]
	v_med3_f32 v54, v54, s81, v170
	v_med3_f32 v55, v55, s81, v170
	v_pk_mul_f32 v[184:185], v[60:61], v[188:189]
	v_rcp_f32_e32 v184, v184
	v_rcp_f32_e32 v185, v185
	s_nop 0
	v_pk_mul_f32 v[186:187], v[184:185], v[188:189]
	v_pk_mul_f32 v[188:189], v[184:185], v[60:61]
	v_pk_mul_f32 v[50:51], v[50:51], v[186:187]
	v_med3_f32 v34, v34, s82, v190
	v_med3_f32 v35, v35, s82, v190
	v_pk_mul_f32 v[50:51], v[50:51], v[54:55]
	v_med3_f32 v54, v56, s81, v170
	v_med3_f32 v55, v57, s81, v170
	v_exp_f32_e64 v56, -v34
	v_exp_f32_e64 v57, -v35
	v_pk_mul_f32 v[52:53], v[52:53], v[188:189]
	v_pk_fma_f32 v[36:37], v[58:59], v[36:37], v[48:49] op_sel_hi:[0,1,1]
	v_pk_mul_f32 v[52:53], v[52:53], v[54:55]
	v_pk_add_f32 v[54:55], v[56:57], 1.0 op_sel_hi:[1,0]
	v_med3_f32 v36, v36, s82, v190
	v_med3_f32 v37, v37, s82, v190
	s_lshl_b32 s10, s10, 5
	v_add3_u32 v109, s67, v42, v142
	v_add_u32_e32 v106, s65, v106
	v_exp_f32_e64 v188, -v36
	v_exp_f32_e64 v189, -v37
	s_lshl_b32 s11, s76, 7
	s_and_b32 s10, s10, 0x60
	ds_read_b128 v[42:45], v109
	v_ashrrev_i32_e32 v107, 31, v106
	s_or_b32 s10, s10, s11
	v_lshlrev_b64 v[110:111], 10, v[106:107]
	v_cvt_pk_fp8_f32 v102, v100, v101 op_sel:[0,0,1]
	v_pk_fma_f32 v[38:39], v[58:59], v[38:39], v[46:47] op_sel_hi:[0,1,1]
	s_ashr_i32 s11, s10, 31
	v_lshl_add_u64 v[110:111], s[18:19], 0, v[110:111]
	v_cvt_pk_fp8_f32 v86, v84, v85 op_sel:[0,0,1]
	v_cvt_pk_fp8_f32 v87, v66, v67 op_sel:[0,0,1]
	v_pk_fma_f32 v[40:41], v[58:59], v[40:41], v[150:151] op_sel_hi:[0,1,1]
	v_med3_f32 v38, v38, s81, v170
	v_med3_f32 v39, v39, s81, v170
	v_lshl_add_u64 v[110:111], v[110:111], 0, s[10:11]
	v_pk_mul_f32 v[34:35], v[34:35], v[38:39]
	v_med3_f32 v38, v40, s81, v170
	v_med3_f32 v39, v41, s81, v170
	v_pk_add_f32 v[188:189], v[188:189], 1.0 op_sel_hi:[1,0]
	v_lshl_add_u64 v[66:67], v[110:111], 0, v[142:143]
	v_pk_mul_f32 v[184:185], v[54:55], v[188:189]
	v_rcp_f32_e32 v184, v184
	v_rcp_f32_e32 v185, v185
	s_nop 0
	v_pk_mul_f32 v[186:187], v[184:185], v[188:189]
	v_pk_mul_f32 v[188:189], v[184:185], v[54:55]
	v_pk_mul_f32 v[34:35], v[34:35], v[186:187]
	s_waitcnt lgkmcnt(0)
	global_store_dwordx4 v[66:67], v[42:45], off
	ds_write_b64 v108, v[102:103]
	ds_write_b64 v108, v[86:87] offset:768
	v_or_b32_e32 v66, 32, v106
	v_mov_b32_e32 v55, v143
	ds_read_b128 v[42:45], v109
	v_ashrrev_i32_e32 v67, 31, v66
	v_cvt_pk_fp8_f32 v55, v34, v35
	v_lshlrev_b64 v[66:67], 10, v[66:67]
	v_lshl_add_u64 v[66:67], s[18:19], 0, v[66:67]
	v_pk_mul_f32 v[34:35], v[36:37], v[188:189]
	v_mul_f32_e32 v40, 0x3d800000, v171
	v_lshl_add_u64 v[66:67], v[66:67], 0, s[10:11]
	v_pk_mul_f32 v[34:35], v[34:35], v[38:39]
	v_pk_fma_f32 v[26:27], v[40:41], v[26:27], v[160:161] op_sel_hi:[0,1,1]
	v_cvt_pk_fp8_f32 v55, v34, v35 op_sel:[0,0,1]
	v_lshl_add_u64 v[34:35], v[66:67], 0, v[142:143]
	v_med3_f32 v26, v26, s82, v190
	v_med3_f32 v27, v27, s82, v190
	s_waitcnt lgkmcnt(0)
	global_store_dwordx4 v[34:35], v[42:45], off
	v_pk_fma_f32 v[28:29], v[40:41], v[28:29], v[154:155] op_sel_hi:[0,1,1]
	v_med3_f32 v28, v28, s82, v190
	v_exp_f32_e64 v42, -v26
	v_exp_f32_e64 v43, -v27
	v_med3_f32 v29, v29, s82, v190
	v_exp_f32_e64 v188, -v28
	v_exp_f32_e64 v189, -v29
	v_pk_add_f32 v[42:43], v[42:43], 1.0 op_sel_hi:[1,0]
	v_pk_fma_f32 v[30:31], v[40:41], v[30:31], v[156:157] op_sel_hi:[0,1,1]
	v_pk_fma_f32 v[18:19], v[40:41], v[18:19], v[152:153] op_sel_hi:[0,1,1]
	v_pk_fma_f32 v[32:33], v[40:41], v[32:33], v[158:159] op_sel_hi:[0,1,1]
	v_med3_f32 v30, v30, s81, v170
	v_pk_add_f32 v[188:189], v[188:189], 1.0 op_sel_hi:[1,0]
	v_med3_f32 v31, v31, s81, v170
	v_pk_mul_f32 v[184:185], v[42:43], v[188:189]
	v_rcp_f32_e32 v184, v184
	v_rcp_f32_e32 v185, v185
	s_nop 0
	v_pk_mul_f32 v[186:187], v[184:185], v[188:189]
	v_pk_mul_f32 v[188:189], v[184:185], v[42:43]
	v_pk_mul_f32 v[26:27], v[26:27], v[186:187]
	v_med3_f32 v18, v18, s82, v190
	v_med3_f32 v19, v19, s82, v190
	v_pk_mul_f32 v[26:27], v[26:27], v[30:31]
	v_med3_f32 v30, v32, s81, v170
	v_med3_f32 v31, v33, s81, v170
	v_exp_f32_e64 v32, -v18
	v_exp_f32_e64 v33, -v19
	v_pk_mul_f32 v[28:29], v[28:29], v[188:189]
	v_pk_fma_f32 v[20:21], v[40:41], v[20:21], v[48:49] op_sel_hi:[0,1,1]
	v_pk_mul_f32 v[28:29], v[28:29], v[30:31]
	v_pk_add_f32 v[30:31], v[32:33], 1.0 op_sel_hi:[1,0]
	v_med3_f32 v20, v20, s82, v190
	v_rcp_f32_e32 v30, v30
	v_rcp_f32_e32 v31, v31
	v_med3_f32 v21, v21, s82, v190
	v_pk_fma_f32 v[22:23], v[40:41], v[22:23], v[46:47] op_sel_hi:[0,1,1]
	v_pk_fma_f32 v[24:25], v[40:41], v[24:25], v[150:151] op_sel_hi:[0,1,1]
	v_pk_mul_f32 v[18:19], v[18:19], v[30:31]
	v_exp_f32_e64 v30, -v20
	v_exp_f32_e64 v31, -v21
	v_med3_f32 v22, v22, s81, v170
	v_med3_f32 v23, v23, s81, v170
	v_pk_mul_f32 v[18:19], v[18:19], v[22:23]
	v_med3_f32 v22, v24, s81, v170
	v_med3_f32 v23, v25, s81, v170
	v_pk_add_f32 v[24:25], v[30:31], 1.0 op_sel_hi:[1,0]
	v_mov_b32_e32 v31, v143
	v_rcp_f32_e32 v24, v24
	v_rcp_f32_e32 v25, v25
	v_cvt_pk_fp8_f32 v31, v18, v19
	v_med3_f32 v78, v78, s81, v170
	v_med3_f32 v79, v79, s81, v170
	v_pk_mul_f32 v[18:19], v[20:21], v[24:25]
	v_pk_mul_f32 v[70:71], v[70:71], v[78:79]
	v_pk_mul_f32 v[18:19], v[18:19], v[22:23]
	v_mov_b32_e32 v68, v143
	v_cvt_pk_fp8_f32 v31, v18, v19 op_sel:[0,0,1]
	v_mul_f32_e32 v18, 0x3d800000, v169
	v_pk_fma_f32 v[10:11], v[18:19], v[10:11], v[160:161] op_sel_hi:[0,1,1]
	v_med3_f32 v10, v10, s82, v190
	v_med3_f32 v11, v11, s82, v190
	v_exp_f32_e64 v20, -v10
	v_exp_f32_e64 v21, -v11
	v_pk_fma_f32 v[12:13], v[18:19], v[12:13], v[154:155] op_sel_hi:[0,1,1]
	v_med3_f32 v12, v12, s82, v190
	v_med3_f32 v13, v13, s82, v190
	v_pk_add_f32 v[20:21], v[20:21], 1.0 op_sel_hi:[1,0]
	v_exp_f32_e64 v188, -v12
	v_exp_f32_e64 v189, -v13
	v_pk_fma_f32 v[14:15], v[18:19], v[14:15], v[156:157] op_sel_hi:[0,1,1]
	v_pk_fma_f32 v[2:3], v[18:19], v[2:3], v[152:153] op_sel_hi:[0,1,1]
	v_pk_add_f32 v[188:189], v[188:189], 1.0 op_sel_hi:[1,0]
	v_pk_fma_f32 v[16:17], v[18:19], v[16:17], v[158:159] op_sel_hi:[0,1,1]
	v_med3_f32 v14, v14, s81, v170
	v_med3_f32 v15, v15, s81, v170
	v_pk_mul_f32 v[184:185], v[20:21], v[188:189]
	v_rcp_f32_e32 v184, v184
	v_rcp_f32_e32 v185, v185
	s_nop 0
	v_pk_mul_f32 v[186:187], v[184:185], v[188:189]
	v_pk_mul_f32 v[188:189], v[184:185], v[20:21]
	v_pk_mul_f32 v[10:11], v[10:11], v[186:187]
	v_med3_f32 v2, v2, s82, v190
	v_med3_f32 v3, v3, s82, v190
	v_pk_mul_f32 v[10:11], v[10:11], v[14:15]
	v_med3_f32 v14, v16, s81, v170
	v_med3_f32 v15, v17, s81, v170
	v_exp_f32_e64 v16, -v2
	v_exp_f32_e64 v17, -v3
	v_pk_mul_f32 v[12:13], v[12:13], v[188:189]
	v_pk_fma_f32 v[4:5], v[18:19], v[4:5], v[48:49] op_sel_hi:[0,1,1]
	v_pk_mul_f32 v[12:13], v[12:13], v[14:15]
	v_pk_add_f32 v[14:15], v[16:17], 1.0 op_sel_hi:[1,0]
	v_med3_f32 v4, v4, s82, v190
	v_med3_f32 v5, v5, s82, v190
	v_cvt_pk_fp8_f32 v68, v70, v71
	v_mov_b32_e32 v54, v143
	v_exp_f32_e64 v188, -v4
	v_exp_f32_e64 v189, -v5
	v_cvt_pk_fp8_f32 v54, v50, v51
	v_med3_f32 v76, v76, s81, v170
	v_med3_f32 v77, v77, s81, v170
	v_pk_fma_f32 v[6:7], v[18:19], v[6:7], v[46:47] op_sel_hi:[0,1,1]
	v_pk_mul_f32 v[72:73], v[72:73], v[76:77]
	v_pk_fma_f32 v[8:9], v[18:19], v[8:9], v[150:151] op_sel_hi:[0,1,1]
	v_med3_f32 v6, v6, s81, v170
	v_med3_f32 v7, v7, s81, v170
	v_cvt_pk_fp8_f32 v68, v72, v73 op_sel:[0,0,1]
	v_pk_mul_f32 v[2:3], v[2:3], v[6:7]
	v_med3_f32 v6, v8, s81, v170
	v_med3_f32 v7, v9, s81, v170
	v_pk_add_f32 v[188:189], v[188:189], 1.0 op_sel_hi:[1,0]
	v_cvt_pk_fp8_f32 v54, v52, v53 op_sel:[0,0,1]
	v_mov_b32_e32 v30, v143
	v_pk_mul_f32 v[184:185], v[14:15], v[188:189]
	v_rcp_f32_e32 v184, v184
	v_rcp_f32_e32 v185, v185
	s_nop 0
	v_pk_mul_f32 v[186:187], v[184:185], v[188:189]
	v_pk_mul_f32 v[188:189], v[184:185], v[14:15]
	v_pk_mul_f32 v[2:3], v[2:3], v[186:187]
	v_cvt_pk_fp8_f32 v30, v26, v27
	v_mov_b32_e32 v14, v143
	v_mov_b32_e32 v15, v143
	v_cvt_pk_fp8_f32 v14, v10, v11
	v_cvt_pk_fp8_f32 v15, v2, v3
	ds_write_b64 v108, v[68:69]
	ds_write_b64 v108, v[54:55] offset:768
	v_add_u32_e32 v38, 0x80, v106
	ds_read_b128 v[34:37], v109
	v_ashrrev_i32_e32 v39, 31, v38
	v_pk_mul_f32 v[2:3], v[4:5], v[188:189]
	v_lshlrev_b64 v[38:39], 10, v[38:39]
	v_cvt_pk_fp8_f32 v30, v28, v29 op_sel:[0,0,1]
	v_pk_mul_f32 v[2:3], v[2:3], v[6:7]
	v_lshl_add_u64 v[38:39], s[18:19], 0, v[38:39]
	v_cvt_pk_fp8_f32 v14, v12, v13 op_sel:[0,0,1]
	v_cvt_pk_fp8_f32 v15, v2, v3 op_sel:[0,0,1]
	v_lshl_add_u64 v[38:39], v[38:39], 0, s[10:11]
	v_lshl_add_u64 v[2:3], v[38:39], 0, v[142:143]
	s_waitcnt lgkmcnt(0)
	global_store_dwordx4 v[2:3], v[34:37], off
	ds_write_b64 v108, v[30:31]
	ds_write_b64 v108, v[14:15] offset:768
	v_add_u32_e32 v6, 0xa0, v106
	ds_read_b128 v[2:5], v109
	v_ashrrev_i32_e32 v7, 31, v6
	v_lshlrev_b64 v[6:7], 10, v[6:7]
	v_lshl_add_u64 v[6:7], s[18:19], 0, v[6:7]
	v_lshl_add_u64 v[6:7], v[6:7], 0, s[10:11]
	v_lshl_add_u64 v[6:7], v[6:7], 0, v[142:143]
	s_and_b64 vcc, exec, s[8:9]
	s_mov_b64 s[8:9], -1
	s_waitcnt lgkmcnt(0)
	global_store_dwordx4 v[6:7], v[2:5], off
	s_cbranch_vccnz .LBB0_3339
	s_lshl_b64 s[8:9], s[70:71], 12
	s_add_u32 s11, s6, s8
	s_addc_u32 s65, s7, s9
	s_lshl_b32 s8, s64, 7
	s_ashr_i32 s9, s8, 31
	v_mov_b32_e32 v2, v0
	s_lshl_b64 s[8:9], s[8:9], 1
	s_add_u32 s8, s11, s8
	v_readfirstlane_b32 s10, v2
	s_addc_u32 s9, s65, s9
	s_and_b32 s11, s10, 0xc0
	s_add_u32 s8, s8, s11
	s_addc_u32 s9, s9, 0
	v_and_b32_e32 v3, 48, v2
	global_load_dwordx4 v[46:49], v3, s[8:9]
	global_load_dwordx4 v[42:45], v3, s[8:9] offset:2048
	s_ashr_i32 s9, s10, 2
	s_lshl_b32 s8, s66, 8
	s_andn2_b32 s9, s9, 63
	s_add_i32 s9, s9, s8
	v_and_or_b32 v2, v2, 15, s9
	v_lshlrev_b32_e32 v4, 2, v2
	global_load_dword v179, v4, s[14:15] offset:0
	global_load_dword v178, v4, s[14:15] offset:64
	global_load_dword v177, v4, s[14:15] offset:128
	global_load_dword v176, v4, s[14:15] offset:192
	global_load_dword v175, v4, s[14:15] offset:512
	global_load_dword v174, v4, s[14:15] offset:576
	global_load_dword v171, v4, s[14:15] offset:640
	global_load_dword v169, v4, s[14:15] offset:704
	s_andn2_b64 vcc, exec, s[16:17]
	s_cbranch_vccnz .LBB0_3338
	s_barrier
	s_branch .LBB0_3338

.LBB0_3429:
	v_lshlrev_b32_e32 v158, 16, v6
	v_and_b32_e32 v159, 0xffff0000, v6
	v_lshlrev_b32_e32 v154, 16, v8
	v_and_b32_e32 v155, 0xffff0000, v8
	v_lshlrev_b32_e32 v156, 16, v7
	v_and_b32_e32 v157, 0xffff0000, v7
	v_lshlrev_b32_e32 v152, 16, v9
	v_and_b32_e32 v153, 0xffff0000, v9
	s_waitcnt vmcnt(10)
	v_lshlrev_b32_e32 v6, 16, v4
	v_and_b32_e32 v7, 0xffff0000, v4
	v_mul_f32_e32 v4, 0x41000000, v146
	v_pk_fma_f32 v[134:135], v[134:135], s[38:39], v[158:159] op_sel_hi:[1,0,1]
	v_pk_fma_f32 v[130:131], v[130:131], s[38:39], v[154:155] op_sel_hi:[1,0,1]
	v_pk_fma_f32 v[136:137], v[136:137], s[38:39], v[156:157] op_sel_hi:[1,0,1]
	v_pk_mul_f32 v[134:135], v[4:5], v[134:135] op_sel_hi:[0,1]
	v_pk_fma_f32 v[132:133], v[132:133], s[38:39], v[152:153] op_sel_hi:[1,0,1]
	v_pk_mul_f32 v[130:131], v[4:5], v[130:131] op_sel_hi:[0,1]
	v_lshlrev_b32_e32 v150, 16, v2
	v_and_b32_e32 v151, 0xffff0000, v2
	v_lshlrev_b32_e32 v8, 16, v3
	v_and_b32_e32 v9, 0xffff0000, v3
	v_lshlrev_b32_e32 v2, 16, v5
	v_and_b32_e32 v3, 0xffff0000, v5
	v_pk_mul_f32 v[136:137], v[4:5], v[136:137] op_sel_hi:[0,1]
	v_pk_mul_f32 v[132:133], v[4:5], v[132:133] op_sel_hi:[0,1]
	v_med3_f32 v5, v134, s75, v164
	v_med3_f32 v134, v130, s75, v164
	v_med3_f32 v135, v135, s75, v164
	v_mov_b32_e32 v130, 0
	v_cvt_pk_fp8_f32 v130, v5, v135
	v_med3_f32 v136, v136, s75, v164
	v_med3_f32 v5, v137, s75, v164
	v_pk_fma_f32 v[126:127], v[126:127], s[38:39], v[150:151] op_sel_hi:[1,0,1]
	v_pk_fma_f32 v[128:129], v[128:129], s[38:39], v[8:9] op_sel_hi:[1,0,1]
	v_pk_fma_f32 v[122:123], v[122:123], s[38:39], v[6:7] op_sel_hi:[1,0,1]
	v_pk_fma_f32 v[124:125], v[124:125], s[38:39], v[2:3] op_sel_hi:[1,0,1]
	v_cvt_pk_fp8_f32 v130, v136, v5 op_sel:[0,0,1]
	v_pk_mul_f32 v[128:129], v[4:5], v[128:129] op_sel_hi:[0,1]
	v_pk_mul_f32 v[126:127], v[4:5], v[126:127] op_sel_hi:[0,1]
	v_pk_mul_f32 v[124:125], v[4:5], v[124:125] op_sel_hi:[0,1]
	v_pk_mul_f32 v[4:5], v[4:5], v[122:123] op_sel_hi:[0,1]
	v_med3_f32 v146, v131, s75, v164
	v_mov_b32_e32 v131, 0
	v_med3_f32 v122, v126, s75, v164
	v_med3_f32 v123, v4, s75, v164
	v_med3_f32 v126, v127, s75, v164
	v_med3_f32 v127, v5, s75, v164
	v_mov_b32_e32 v4, 0
	v_mov_b32_e32 v5, 0
	v_cvt_pk_fp8_f32 v131, v134, v146
	v_cvt_pk_fp8_f32 v4, v122, v126
	v_cvt_pk_fp8_f32 v5, v123, v127
	v_mov_b32_e32 v171, v0
	v_med3_f32 v132, v132, s75, v164
	v_readfirstlane_b32 s41, v171
	s_lshr_b32 s8, s41, 6
	v_med3_f32 v133, v133, s75, v164
	v_med3_f32 v128, v128, s75, v164
	v_med3_f32 v124, v124, s75, v164
	v_med3_f32 v122, v129, s75, v164
	v_med3_f32 v123, v125, s75, v164
	s_mulk_i32 s8, 0xb00
	v_cvt_pk_fp8_f32 v131, v132, v133 op_sel:[0,0,1]
	v_cvt_pk_fp8_f32 v4, v128, v122 op_sel:[0,0,1]
	v_cvt_pk_fp8_f32 v5, v124, v123 op_sel:[0,0,1]
	s_add_i32 s8, s8, 0
	v_and_b32_e32 v172, 15, v171
	v_lshrrev_b32_e32 v123, 1, v171
	s_add_i32 s43, s8, 0x20000
	v_mul_u32_u24_e32 v122, 0x50, v172
	v_and_b32_e32 v123, 24, v123
	v_add3_u32 v122, s43, v122, v123
	s_and_b32 s9, s41, 0xc0
	ds_write2_b64 v122, v[130:131], v[4:5] offset1:4
	v_bfe_u32 v4, v171, 2, 4
	s_ashr_i32 s41, s41, 2
	v_mul_u32_u24_e32 v5, 0x50, v4
	v_lshlrev_b32_e32 v123, 4, v171
	s_andn2_b32 s41, s41, 63
	v_lshl_or_b32 v4, s50, 8, v4
	v_and_b32_e32 v146, 48, v123
	v_add_u32_e32 v4, s41, v4
	v_mul_f32_e32 v130, 0x41000000, v170
	v_pk_fma_f32 v[118:119], v[118:119], s[38:39], v[158:159] op_sel_hi:[1,0,1]
	v_pk_fma_f32 v[114:115], v[114:115], s[38:39], v[154:155] op_sel_hi:[1,0,1]
	v_add3_u32 v123, s43, v5, v146
	v_ashrrev_i32_e32 v5, 31, v4
	v_pk_mul_f32 v[118:119], v[130:131], v[118:119] op_sel_hi:[0,1]
	v_pk_mul_f32 v[114:115], v[130:131], v[114:115] op_sel_hi:[0,1]
	v_lshlrev_b64 v[128:129], 10, v[4:5]
	v_med3_f32 v5, v118, s75, v164
	v_med3_f32 v118, v114, s75, v164
	v_med3_f32 v119, v119, s75, v164
	v_mov_b32_e32 v114, v147
	v_cvt_pk_fp8_f32 v114, v5, v119
	v_pk_fma_f32 v[120:121], v[120:121], s[38:39], v[156:157] op_sel_hi:[1,0,1]
	v_pk_fma_f32 v[116:117], v[116:117], s[38:39], v[152:153] op_sel_hi:[1,0,1]
	v_pk_mul_f32 v[120:121], v[130:131], v[120:121] op_sel_hi:[0,1]
	v_pk_mul_f32 v[116:117], v[130:131], v[116:117] op_sel_hi:[0,1]
	v_med3_f32 v131, v115, s75, v164
	v_pk_fma_f32 v[110:111], v[110:111], s[38:39], v[150:151] op_sel_hi:[1,0,1]
	v_pk_fma_f32 v[106:107], v[106:107], s[38:39], v[6:7] op_sel_hi:[1,0,1]
	v_med3_f32 v120, v120, s75, v164
	v_med3_f32 v5, v121, s75, v164
	v_pk_mul_f32 v[110:111], v[130:131], v[110:111] op_sel_hi:[0,1]
	v_pk_mul_f32 v[106:107], v[130:131], v[106:107] op_sel_hi:[0,1]
	v_cvt_pk_fp8_f32 v114, v120, v5 op_sel:[0,0,1]
	v_med3_f32 v5, v110, s75, v164
	v_med3_f32 v110, v106, s75, v164
	v_med3_f32 v111, v111, s75, v164
	v_mov_b32_e32 v106, v147
	v_cvt_pk_fp8_f32 v106, v5, v111
	v_pk_fma_f32 v[112:113], v[112:113], s[38:39], v[8:9] op_sel_hi:[1,0,1]
	v_mov_b32_e32 v115, v147
	v_pk_mul_f32 v[112:113], v[130:131], v[112:113] op_sel_hi:[0,1]
	v_med3_f32 v112, v112, s75, v164
	v_med3_f32 v5, v113, s75, v164
	v_cvt_pk_fp8_f32 v106, v112, v5 op_sel:[0,0,1]
	v_mul_f32_e32 v112, 0x41000000, v169
	v_pk_fma_f32 v[102:103], v[102:103], s[38:39], v[158:159] op_sel_hi:[1,0,1]
	v_pk_fma_f32 v[98:99], v[98:99], s[38:39], v[154:155] op_sel_hi:[1,0,1]
	v_cvt_pk_fp8_f32 v115, v118, v131
	v_pk_mul_f32 v[102:103], v[112:113], v[102:103] op_sel_hi:[0,1]
	v_pk_mul_f32 v[98:99], v[112:113], v[98:99] op_sel_hi:[0,1]
	v_med3_f32 v5, v102, s75, v164
	v_med3_f32 v102, v98, s75, v164
	v_med3_f32 v103, v103, s75, v164
	v_mov_b32_e32 v98, v147
	v_cvt_pk_fp8_f32 v98, v5, v103
	v_med3_f32 v116, v116, s75, v164
	v_med3_f32 v117, v117, s75, v164
	v_pk_fma_f32 v[104:105], v[104:105], s[38:39], v[156:157] op_sel_hi:[1,0,1]
	v_pk_fma_f32 v[100:101], v[100:101], s[38:39], v[152:153] op_sel_hi:[1,0,1]
	v_cvt_pk_fp8_f32 v115, v116, v117 op_sel:[0,0,1]
	v_med3_f32 v116, v107, s75, v164
	v_mov_b32_e32 v107, v147
	v_pk_mul_f32 v[104:105], v[112:113], v[104:105] op_sel_hi:[0,1]
	v_pk_mul_f32 v[100:101], v[112:113], v[100:101] op_sel_hi:[0,1]
	v_med3_f32 v113, v99, s75, v164
	v_pk_fma_f32 v[94:95], v[94:95], s[38:39], v[150:151] op_sel_hi:[1,0,1]
	v_pk_fma_f32 v[90:91], v[90:91], s[38:39], v[6:7] op_sel_hi:[1,0,1]
	v_cvt_pk_fp8_f32 v107, v110, v116
	v_med3_f32 v104, v104, s75, v164
	v_med3_f32 v5, v105, s75, v164
	v_pk_mul_f32 v[94:95], v[112:113], v[94:95] op_sel_hi:[0,1]
	v_pk_mul_f32 v[90:91], v[112:113], v[90:91] op_sel_hi:[0,1]
	v_pk_fma_f32 v[108:109], v[108:109], s[38:39], v[2:3] op_sel_hi:[1,0,1]
	v_mov_b32_e32 v99, v147
	v_cvt_pk_fp8_f32 v98, v104, v5 op_sel:[0,0,1]
	v_med3_f32 v5, v94, s75, v164
	v_med3_f32 v94, v90, s75, v164
	v_med3_f32 v95, v95, s75, v164
	v_mov_b32_e32 v90, v147
	s_lshl_b32 s8, s62, 8
	ds_read_b128 v[124:127], v123
	v_pk_mul_f32 v[108:109], v[130:131], v[108:109] op_sel_hi:[0,1]
	v_cvt_pk_fp8_f32 v99, v102, v113
	v_cvt_pk_fp8_f32 v90, v5, v95
	s_or_b32 s8, s9, s8
	v_med3_f32 v108, v108, s75, v164
	v_med3_f32 v109, v109, s75, v164
	v_pk_fma_f32 v[96:97], v[96:97], s[38:39], v[8:9] op_sel_hi:[1,0,1]
	s_ashr_i32 s9, s8, 31
	v_lshl_add_u64 v[128:129], s[16:17], 0, v[128:129]
	v_cvt_pk_fp8_f32 v107, v108, v109 op_sel:[0,0,1]
	v_pk_mul_f32 v[96:97], v[112:113], v[96:97] op_sel_hi:[0,1]
	v_lshl_add_u64 v[128:129], v[128:129], 0, s[8:9]
	v_med3_f32 v100, v100, s75, v164
	v_med3_f32 v101, v101, s75, v164
	v_med3_f32 v96, v96, s75, v164
	v_med3_f32 v5, v97, s75, v164
	v_lshl_add_u64 v[108:109], v[128:129], 0, v[146:147]
	v_cvt_pk_fp8_f32 v99, v100, v101 op_sel:[0,0,1]
	v_med3_f32 v100, v91, s75, v164
	v_mov_b32_e32 v91, v147
	v_cvt_pk_fp8_f32 v90, v96, v5 op_sel:[0,0,1]
	v_mul_f32_e32 v96, 0x41000000, v168
	v_pk_fma_f32 v[78:79], v[78:79], s[38:39], v[158:159] op_sel_hi:[1,0,1]
	v_pk_fma_f32 v[74:75], v[74:75], s[38:39], v[154:155] op_sel_hi:[1,0,1]
	s_waitcnt lgkmcnt(0)
	global_store_dwordx4 v[108:109], v[124:127], off
	v_cvt_pk_fp8_f32 v91, v94, v100
	v_pk_fma_f32 v[80:81], v[80:81], s[38:39], v[156:157] op_sel_hi:[1,0,1]
	v_pk_mul_f32 v[78:79], v[96:97], v[78:79] op_sel_hi:[0,1]
	v_pk_fma_f32 v[76:77], v[76:77], s[38:39], v[152:153] op_sel_hi:[1,0,1]
	v_pk_mul_f32 v[74:75], v[96:97], v[74:75] op_sel_hi:[0,1]
	ds_write2_b64 v122, v[114:115], v[106:107] offset1:4
	v_or_b32_e32 v110, 16, v4
	v_pk_fma_f32 v[92:93], v[92:93], s[38:39], v[2:3] op_sel_hi:[1,0,1]
	v_pk_mul_f32 v[80:81], v[96:97], v[80:81] op_sel_hi:[0,1]
	v_pk_mul_f32 v[76:77], v[96:97], v[76:77] op_sel_hi:[0,1]
	v_med3_f32 v5, v78, s75, v164
	v_med3_f32 v78, v74, s75, v164
	v_med3_f32 v79, v79, s75, v164
	v_med3_f32 v97, v75, s75, v164
	v_mov_b32_e32 v74, v147
	v_mov_b32_e32 v75, v147
	ds_read_b128 v[106:109], v123
	v_ashrrev_i32_e32 v111, 31, v110
	v_pk_mul_f32 v[92:93], v[112:113], v[92:93] op_sel_hi:[0,1]
	v_cvt_pk_fp8_f32 v74, v5, v79
	v_cvt_pk_fp8_f32 v75, v78, v97
	v_lshlrev_b64 v[110:111], 10, v[110:111]
	v_med3_f32 v92, v92, s75, v164
	v_med3_f32 v93, v93, s75, v164
	v_lshl_add_u64 v[110:111], s[16:17], 0, v[110:111]
	v_cvt_pk_fp8_f32 v91, v92, v93 op_sel:[0,0,1]
	v_pk_fma_f32 v[62:63], v[62:63], s[38:39], v[150:151] op_sel_hi:[1,0,1]
	v_pk_fma_f32 v[58:59], v[58:59], s[38:39], v[6:7] op_sel_hi:[1,0,1]
	v_lshl_add_u64 v[110:111], v[110:111], 0, s[8:9]
	v_med3_f32 v80, v80, s75, v164
	v_med3_f32 v76, v76, s75, v164
	v_med3_f32 v5, v81, s75, v164
	v_med3_f32 v77, v77, s75, v164
	v_pk_mul_f32 v[62:63], v[96:97], v[62:63] op_sel_hi:[0,1]
	v_pk_mul_f32 v[58:59], v[96:97], v[58:59] op_sel_hi:[0,1]
	v_lshl_add_u64 v[92:93], v[110:111], 0, v[146:147]
	v_cvt_pk_fp8_f32 v74, v80, v5 op_sel:[0,0,1]
	v_cvt_pk_fp8_f32 v75, v76, v77 op_sel:[0,0,1]
	v_med3_f32 v5, v62, s75, v164
	v_med3_f32 v62, v58, s75, v164
	v_med3_f32 v63, v63, s75, v164
	v_med3_f32 v76, v59, s75, v164
	v_mov_b32_e32 v58, v147
	v_mov_b32_e32 v59, v147
	s_waitcnt lgkmcnt(0)
	global_store_dwordx4 v[92:93], v[106:109], off
	v_cvt_pk_fp8_f32 v58, v5, v63
	v_cvt_pk_fp8_f32 v59, v62, v76
	ds_write2_b64 v122, v[98:99], v[90:91] offset1:4
	v_or_b32_e32 v94, 32, v4
	v_pk_fma_f32 v[64:65], v[64:65], s[38:39], v[8:9] op_sel_hi:[1,0,1]
	v_pk_fma_f32 v[60:61], v[60:61], s[38:39], v[2:3] op_sel_hi:[1,0,1]
	ds_read_b128 v[90:93], v123
	v_ashrrev_i32_e32 v95, 31, v94
	v_pk_mul_f32 v[64:65], v[96:97], v[64:65] op_sel_hi:[0,1]
	v_pk_mul_f32 v[60:61], v[96:97], v[60:61] op_sel_hi:[0,1]
	v_lshlrev_b64 v[94:95], 10, v[94:95]
	v_med3_f32 v64, v64, s75, v164
	v_med3_f32 v60, v60, s75, v164
	v_med3_f32 v5, v65, s75, v164
	v_med3_f32 v61, v61, s75, v164
	v_lshl_add_u64 v[94:95], s[16:17], 0, v[94:95]
	v_cvt_pk_fp8_f32 v58, v64, v5 op_sel:[0,0,1]
	v_cvt_pk_fp8_f32 v59, v60, v61 op_sel:[0,0,1]
	v_lshl_add_u64 v[94:95], v[94:95], 0, s[8:9]
	v_lshl_add_u64 v[60:61], v[94:95], 0, v[146:147]
	s_waitcnt lgkmcnt(0)
	global_store_dwordx4 v[60:61], v[90:93], off
	ds_write2_b64 v122, v[74:75], v[58:59] offset1:4
	v_mul_f32_e32 v64, 0x41000000, v167
	v_pk_fma_f32 v[74:75], v[86:87], s[38:39], v[158:159] op_sel_hi:[1,0,1]
	v_pk_fma_f32 v[78:79], v[82:83], s[38:39], v[154:155] op_sel_hi:[1,0,1]
	v_pk_mul_f32 v[74:75], v[64:65], v[74:75] op_sel_hi:[0,1]
	v_pk_fma_f32 v[76:77], v[88:89], s[38:39], v[156:157] op_sel_hi:[1,0,1]
	v_pk_fma_f32 v[80:81], v[84:85], s[38:39], v[152:153] op_sel_hi:[1,0,1]
	v_pk_mul_f32 v[78:79], v[64:65], v[78:79] op_sel_hi:[0,1]
	v_med3_f32 v5, v74, s75, v164
	v_med3_f32 v75, v75, s75, v164
	v_mov_b32_e32 v74, v147
	v_pk_mul_f32 v[76:77], v[64:65], v[76:77] op_sel_hi:[0,1]
	v_pk_mul_f32 v[80:81], v[64:65], v[80:81] op_sel_hi:[0,1]
	v_med3_f32 v65, v78, s75, v164
	v_med3_f32 v78, v79, s75, v164
	v_cvt_pk_fp8_f32 v74, v5, v75
	v_mov_b32_e32 v75, v147
	v_cvt_pk_fp8_f32 v75, v65, v78
	v_med3_f32 v79, v80, s75, v164
	v_med3_f32 v65, v81, s75, v164
	v_pk_fma_f32 v[70:71], v[70:71], s[38:39], v[150:151] op_sel_hi:[1,0,1]
	v_pk_fma_f32 v[72:73], v[72:73], s[38:39], v[8:9] op_sel_hi:[1,0,1]
	v_pk_fma_f32 v[66:67], v[66:67], s[38:39], v[6:7] op_sel_hi:[1,0,1]
	v_pk_fma_f32 v[68:69], v[68:69], s[38:39], v[2:3] op_sel_hi:[1,0,1]
	v_med3_f32 v76, v76, s75, v164
	v_med3_f32 v5, v77, s75, v164
	v_cvt_pk_fp8_f32 v75, v79, v65 op_sel:[0,0,1]
	v_pk_mul_f32 v[72:73], v[64:65], v[72:73] op_sel_hi:[0,1]
	v_pk_mul_f32 v[70:71], v[64:65], v[70:71] op_sel_hi:[0,1]
	v_pk_mul_f32 v[68:69], v[64:65], v[68:69] op_sel_hi:[0,1]
	v_pk_mul_f32 v[64:65], v[64:65], v[66:67] op_sel_hi:[0,1]
	v_cvt_pk_fp8_f32 v74, v76, v5 op_sel:[0,0,1]
	v_med3_f32 v5, v70, s75, v164
	v_med3_f32 v66, v64, s75, v164
	v_med3_f32 v67, v71, s75, v164
	v_med3_f32 v70, v65, s75, v164
	v_mov_b32_e32 v64, v147
	v_mov_b32_e32 v65, v147
	v_cvt_pk_fp8_f32 v64, v5, v67
	v_cvt_pk_fp8_f32 v65, v66, v70
	v_or_b32_e32 v62, 48, v4
	ds_read_b128 v[58:61], v123
	v_ashrrev_i32_e32 v63, 31, v62
	v_lshlrev_b64 v[62:63], 10, v[62:63]
	v_med3_f32 v71, v72, s75, v164
	v_med3_f32 v68, v68, s75, v164
	v_med3_f32 v5, v73, s75, v164
	v_med3_f32 v66, v69, s75, v164
	v_lshl_add_u64 v[62:63], s[16:17], 0, v[62:63]
	v_cvt_pk_fp8_f32 v64, v71, v5 op_sel:[0,0,1]
	v_cvt_pk_fp8_f32 v65, v68, v66 op_sel:[0,0,1]
	v_lshl_add_u64 v[62:63], v[62:63], 0, s[8:9]
	v_lshl_add_u64 v[62:63], v[62:63], 0, v[146:147]
	s_waitcnt lgkmcnt(0)
	global_store_dwordx4 v[62:63], v[58:61], off
	ds_write2_b64 v122, v[74:75], v[64:65] offset1:4
	v_mul_f32_e32 v64, 0x41000000, v166
	v_pk_fma_f32 v[54:55], v[54:55], s[38:39], v[158:159] op_sel_hi:[1,0,1]
	v_pk_fma_f32 v[50:51], v[50:51], s[38:39], v[154:155] op_sel_hi:[1,0,1]
	v_pk_mul_f32 v[54:55], v[64:65], v[54:55] op_sel_hi:[0,1]
	v_pk_mul_f32 v[50:51], v[64:65], v[50:51] op_sel_hi:[0,1]
	v_med3_f32 v5, v54, s75, v164
	v_med3_f32 v54, v50, s75, v164
	v_med3_f32 v55, v55, s75, v164
	v_mov_b32_e32 v50, v147
	v_cvt_pk_fp8_f32 v50, v5, v55
	v_pk_fma_f32 v[56:57], v[56:57], s[38:39], v[156:157] op_sel_hi:[1,0,1]
	v_pk_fma_f32 v[52:53], v[52:53], s[38:39], v[152:153] op_sel_hi:[1,0,1]
	v_pk_mul_f32 v[56:57], v[64:65], v[56:57] op_sel_hi:[0,1]
	v_pk_mul_f32 v[52:53], v[64:65], v[52:53] op_sel_hi:[0,1]
	v_med3_f32 v65, v51, s75, v164
	v_pk_fma_f32 v[46:47], v[46:47], s[38:39], v[150:151] op_sel_hi:[1,0,1]
	v_pk_fma_f32 v[42:43], v[42:43], s[38:39], v[6:7] op_sel_hi:[1,0,1]
	v_med3_f32 v56, v56, s75, v164
	v_med3_f32 v5, v57, s75, v164
	v_pk_mul_f32 v[46:47], v[64:65], v[46:47] op_sel_hi:[0,1]
	v_pk_mul_f32 v[42:43], v[64:65], v[42:43] op_sel_hi:[0,1]
	v_cvt_pk_fp8_f32 v50, v56, v5 op_sel:[0,0,1]
	v_med3_f32 v5, v46, s75, v164
	v_med3_f32 v46, v42, s75, v164
	v_med3_f32 v47, v47, s75, v164
	v_mov_b32_e32 v42, v147
	v_cvt_pk_fp8_f32 v42, v5, v47
	v_pk_fma_f32 v[48:49], v[48:49], s[38:39], v[8:9] op_sel_hi:[1,0,1]
	v_mov_b32_e32 v51, v147
	v_pk_mul_f32 v[48:49], v[64:65], v[48:49] op_sel_hi:[0,1]
	v_med3_f32 v48, v48, s75, v164
	v_med3_f32 v5, v49, s75, v164
	v_cvt_pk_fp8_f32 v42, v48, v5 op_sel:[0,0,1]
	v_mul_f32_e32 v48, 0x41000000, v165
	v_pk_fma_f32 v[38:39], v[38:39], s[38:39], v[158:159] op_sel_hi:[1,0,1]
	v_pk_fma_f32 v[34:35], v[34:35], s[38:39], v[154:155] op_sel_hi:[1,0,1]
	v_cvt_pk_fp8_f32 v51, v54, v65
	v_pk_mul_f32 v[38:39], v[48:49], v[38:39] op_sel_hi:[0,1]
	v_pk_mul_f32 v[34:35], v[48:49], v[34:35] op_sel_hi:[0,1]
	v_med3_f32 v5, v38, s75, v164
	v_med3_f32 v38, v34, s75, v164
	v_med3_f32 v39, v39, s75, v164
	v_mov_b32_e32 v34, v147
	v_cvt_pk_fp8_f32 v34, v5, v39
	v_med3_f32 v52, v52, s75, v164
	v_med3_f32 v53, v53, s75, v164
	v_pk_fma_f32 v[40:41], v[40:41], s[38:39], v[156:157] op_sel_hi:[1,0,1]
	v_pk_fma_f32 v[36:37], v[36:37], s[38:39], v[152:153] op_sel_hi:[1,0,1]
	v_cvt_pk_fp8_f32 v51, v52, v53 op_sel:[0,0,1]
	v_med3_f32 v52, v43, s75, v164
	v_mov_b32_e32 v43, v147
	v_pk_mul_f32 v[40:41], v[48:49], v[40:41] op_sel_hi:[0,1]
	v_pk_mul_f32 v[36:37], v[48:49], v[36:37] op_sel_hi:[0,1]
	v_med3_f32 v49, v35, s75, v164
	v_pk_fma_f32 v[30:31], v[30:31], s[38:39], v[150:151] op_sel_hi:[1,0,1]
	v_pk_fma_f32 v[26:27], v[26:27], s[38:39], v[6:7] op_sel_hi:[1,0,1]
	v_cvt_pk_fp8_f32 v43, v46, v52
	v_med3_f32 v40, v40, s75, v164
	v_med3_f32 v5, v41, s75, v164
	v_pk_mul_f32 v[30:31], v[48:49], v[30:31] op_sel_hi:[0,1]
	v_pk_mul_f32 v[26:27], v[48:49], v[26:27] op_sel_hi:[0,1]
	v_add_u32_e32 v62, 0x80, v4
	v_pk_fma_f32 v[44:45], v[44:45], s[38:39], v[2:3] op_sel_hi:[1,0,1]
	v_mov_b32_e32 v35, v147
	v_cvt_pk_fp8_f32 v34, v40, v5 op_sel:[0,0,1]
	v_med3_f32 v5, v30, s75, v164
	v_med3_f32 v30, v26, s75, v164
	v_med3_f32 v31, v31, s75, v164
	v_mov_b32_e32 v26, v147
	ds_read_b128 v[58:61], v123
	v_ashrrev_i32_e32 v63, 31, v62
	v_pk_mul_f32 v[44:45], v[64:65], v[44:45] op_sel_hi:[0,1]
	v_cvt_pk_fp8_f32 v35, v38, v49
	v_cvt_pk_fp8_f32 v26, v5, v31
	v_lshlrev_b64 v[62:63], 10, v[62:63]
	v_med3_f32 v44, v44, s75, v164
	v_med3_f32 v45, v45, s75, v164
	v_pk_fma_f32 v[32:33], v[32:33], s[38:39], v[8:9] op_sel_hi:[1,0,1]
	v_lshl_add_u64 v[62:63], s[16:17], 0, v[62:63]
	v_cvt_pk_fp8_f32 v43, v44, v45 op_sel:[0,0,1]
	v_pk_mul_f32 v[32:33], v[48:49], v[32:33] op_sel_hi:[0,1]
	v_lshl_add_u64 v[62:63], v[62:63], 0, s[8:9]
	v_med3_f32 v36, v36, s75, v164
	v_med3_f32 v37, v37, s75, v164
	v_med3_f32 v32, v32, s75, v164
	v_med3_f32 v5, v33, s75, v164
	v_lshl_add_u64 v[44:45], v[62:63], 0, v[146:147]
	v_cvt_pk_fp8_f32 v35, v36, v37 op_sel:[0,0,1]
	v_med3_f32 v36, v27, s75, v164
	v_mov_b32_e32 v27, v147
	v_cvt_pk_fp8_f32 v26, v32, v5 op_sel:[0,0,1]
	v_mul_f32_e32 v32, 0x41000000, v1
	v_pk_fma_f32 v[22:23], v[22:23], s[38:39], v[158:159] op_sel_hi:[1,0,1]
	v_pk_fma_f32 v[18:19], v[18:19], s[38:39], v[154:155] op_sel_hi:[1,0,1]
	s_waitcnt lgkmcnt(0)
	global_store_dwordx4 v[44:45], v[58:61], off
	v_cvt_pk_fp8_f32 v27, v30, v36
	v_pk_mul_f32 v[22:23], v[32:33], v[22:23] op_sel_hi:[0,1]
	v_pk_mul_f32 v[18:19], v[32:33], v[18:19] op_sel_hi:[0,1]
	ds_write2_b64 v122, v[50:51], v[42:43] offset1:4
	v_add_u32_e32 v46, 0x90, v4
	v_pk_fma_f32 v[28:29], v[28:29], s[38:39], v[2:3] op_sel_hi:[1,0,1]
	v_med3_f32 v1, v22, s75, v164
	v_med3_f32 v5, v18, s75, v164
	v_med3_f32 v22, v23, s75, v164
	v_med3_f32 v23, v19, s75, v164
	v_mov_b32_e32 v18, v147
	v_mov_b32_e32 v19, v147
	ds_read_b128 v[42:45], v123
	v_ashrrev_i32_e32 v47, 31, v46
	v_pk_mul_f32 v[28:29], v[48:49], v[28:29] op_sel_hi:[0,1]
	v_cvt_pk_fp8_f32 v18, v1, v22
	v_cvt_pk_fp8_f32 v19, v5, v23
	v_lshlrev_b64 v[46:47], 10, v[46:47]
	v_med3_f32 v28, v28, s75, v164
	v_med3_f32 v29, v29, s75, v164
	v_pk_fma_f32 v[24:25], v[24:25], s[38:39], v[156:157] op_sel_hi:[1,0,1]
	v_pk_fma_f32 v[20:21], v[20:21], s[38:39], v[152:153] op_sel_hi:[1,0,1]
	v_lshl_add_u64 v[46:47], s[16:17], 0, v[46:47]
	v_cvt_pk_fp8_f32 v27, v28, v29 op_sel:[0,0,1]
	v_pk_mul_f32 v[24:25], v[32:33], v[24:25] op_sel_hi:[0,1]
	v_pk_mul_f32 v[20:21], v[32:33], v[20:21] op_sel_hi:[0,1]
	v_pk_fma_f32 v[14:15], v[14:15], s[38:39], v[150:151] op_sel_hi:[1,0,1]
	v_pk_fma_f32 v[6:7], v[10:11], s[38:39], v[6:7] op_sel_hi:[1,0,1]
	v_lshl_add_u64 v[46:47], v[46:47], 0, s[8:9]
	v_med3_f32 v24, v24, s75, v164
	v_med3_f32 v20, v20, s75, v164
	v_med3_f32 v1, v25, s75, v164
	v_med3_f32 v5, v21, s75, v164
	v_pk_mul_f32 v[14:15], v[32:33], v[14:15] op_sel_hi:[0,1]
	v_pk_mul_f32 v[6:7], v[32:33], v[6:7] op_sel_hi:[0,1]
	v_lshl_add_u64 v[28:29], v[46:47], 0, v[146:147]
	v_cvt_pk_fp8_f32 v18, v24, v1 op_sel:[0,0,1]
	v_cvt_pk_fp8_f32 v19, v20, v5 op_sel:[0,0,1]
	v_med3_f32 v1, v14, s75, v164
	v_med3_f32 v5, v6, s75, v164
	v_med3_f32 v10, v15, s75, v164
	v_med3_f32 v11, v7, s75, v164
	v_mov_b32_e32 v6, v147
	v_mov_b32_e32 v7, v147
	s_waitcnt lgkmcnt(0)
	global_store_dwordx4 v[28:29], v[42:45], off
	v_cvt_pk_fp8_f32 v6, v1, v10
	v_cvt_pk_fp8_f32 v7, v5, v11
	ds_write2_b64 v122, v[34:35], v[26:27] offset1:4
	v_add_u32_e32 v30, 0xa0, v4
	v_pk_fma_f32 v[8:9], v[16:17], s[38:39], v[8:9] op_sel_hi:[1,0,1]
	v_pk_fma_f32 v[2:3], v[12:13], s[38:39], v[2:3] op_sel_hi:[1,0,1]
	ds_read_b128 v[26:29], v123
	v_ashrrev_i32_e32 v31, 31, v30
	v_pk_mul_f32 v[8:9], v[32:33], v[8:9] op_sel_hi:[0,1]
	v_pk_mul_f32 v[2:3], v[32:33], v[2:3] op_sel_hi:[0,1]
	v_lshlrev_b64 v[30:31], 10, v[30:31]
	v_med3_f32 v8, v8, s75, v164
	v_med3_f32 v2, v2, s75, v164
	v_med3_f32 v1, v9, s75, v164
	v_med3_f32 v3, v3, s75, v164
	v_lshl_add_u64 v[30:31], s[16:17], 0, v[30:31]
	v_cvt_pk_fp8_f32 v6, v8, v1 op_sel:[0,0,1]
	v_cvt_pk_fp8_f32 v7, v2, v3 op_sel:[0,0,1]
	v_lshl_add_u64 v[30:31], v[30:31], 0, s[8:9]
	v_lshl_add_u64 v[2:3], v[30:31], 0, v[146:147]
	s_waitcnt lgkmcnt(0)
	global_store_dwordx4 v[2:3], v[26:29], off
	ds_write2_b64 v122, v[18:19], v[6:7] offset1:4
	v_add_u32_e32 v2, 0xb0, v4
	ds_read_b128 v[6:9], v123
	v_ashrrev_i32_e32 v3, 31, v2
	v_lshlrev_b64 v[2:3], 10, v[2:3]
	v_lshl_add_u64 v[2:3], s[16:17], 0, v[2:3]
	v_lshl_add_u64 v[2:3], v[2:3], 0, s[8:9]
	v_lshl_add_u64 v[2:3], v[2:3], 0, v[146:147]
	s_waitcnt lgkmcnt(0)
	global_store_dwordx4 v[2:3], v[6:9], off
	s_and_b64 vcc, exec, s[10:11]
	s_mov_b64 s[8:9], -1
	s_cbranch_vccnz .LBB0_3418
	v_mov_b32_e32 v12, v0
	s_lshl_b32 s9, s42, 8
	v_readfirstlane_b32 s8, v12
	s_and_b32 s10, s8, 0xc0
	s_ashr_i32 s8, s8, 2
	s_andn2_b32 s8, s8, 63
	s_add_i32 s8, s8, s9
	v_and_or_b32 v2, v12, 15, s8
	v_lshlrev_b32_e32 v4, 2, v2
	s_lshl_b64 s[8:9], s[44:45], 11
	s_add_u32 s11, s54, s8
	s_addc_u32 s41, s55, s9
	s_lshl_b32 s8, s40, 8
	global_load_dword v146, v4, s[12:13] offset:0
	global_load_dword v170, v4, s[12:13] offset:64
	global_load_dword v169, v4, s[12:13] offset:128
	global_load_dword v168, v4, s[12:13] offset:192
	global_load_dword v167, v4, s[12:13] offset:512
	global_load_dword v166, v4, s[12:13] offset:576
	global_load_dword v165, v4, s[12:13] offset:640
	global_load_dword v1, v4, s[12:13] offset:704
	s_ashr_i32 s9, s8, 31
	s_lshl_b64 s[8:9], s[8:9], 1
	s_add_u32 s8, s11, s8
	s_addc_u32 s9, s41, s9
	s_lshl_b32 s10, s10, 1
	s_add_u32 s8, s8, s10
	s_addc_u32 s9, s9, 0
	v_and_b32_e32 v2, 48, v12
	global_load_dwordx4 v[6:9], v2, s[8:9]
	s_nop 0
	global_load_dwordx4 v[2:5], v2, s[8:9] offset:64
	s_andn2_b64 vcc, exec, s[14:15]
	s_cbranch_vccnz .LBB0_3417
	s_barrier
	s_branch .LBB0_3417
